# pooling-mixer differences for positions >= 16 rewritten: one lane produces 8 consecutive positions of an 8-column block from w+7 row loads (sliding f32 window sums) instead of w loads per position; po
# speedup vs baseline: 1.0126x; 1.0107x over previous
; __device__ __forceinline__ int fresh_tid() { int t = threadIdx.x; asm volatile("" : "+v"(t)); return t; }
; __device__ __forceinline__ int fresh_bx() { int t = blockIdx.x; asm volatile("" : "+s"(t)); return t; }
; __device__ __forceinline__ void pool_diffs(const bf16_t* Z, bf16_t* DP, int G) {
;     const int gid = fresh_bx() * NTHR + fresh_tid(), NT = G * NTHR;
;     for (int it = gid; it < T * 128; it += NT) {
;         const int t = it >> 7, col = (it & 127) * 8, w = 2 << (col >> 8), cnt = (t + 1 < w) ? t + 1 : w;
.LBB0_398:
	s_mov_b32 s10, s18
	s_waitcnt vmcnt(0)
	v_mov_b32_e32 v2, v0
	s_mov_b32 s8, 0x800
	v_lshl_add_u32 v1, s10, 9, v2
	v_cmp_gt_i32_e32 vcc, s8, v1
	s_and_saveexec_b64 s[8:9], vcc
	s_cbranch_execz .LBB0_433
	s_add_u32 s6, s6, 0x42800000
	v_lshlrev_b32_e32 v2, 3, v2
	s_addc_u32 s7, s7, 0
	s_lshl_b32 s14, s17, 9
	v_lshl_add_u32 v72, s10, 12, v2
	s_lshl_b32 s15, s17, 12
	s_mov_b64 s[10:11], 0
	v_mov_b32_e32 v67, 0
	s_movk_i32 s17, 0x2800
	s_mov_b32 s20, 0x7ff
	s_branch .LBB0_401

; __device__ __forceinline__ int fresh_tid() { int t = threadIdx.x; asm volatile("" : "+v"(t)); return t; }
; __device__ __forceinline__ int fresh_bx() { int t = blockIdx.x; asm volatile("" : "+s"(t)); return t; }
; __device__ __forceinline__ void pool_diffs(const bf16_t* Z, bf16_t* DP, int G) {
;     const int gid = fresh_bx() * NTHR + fresh_tid(), NT = G * NTHR;
;     for (int it = gid; it < T * 128; it += NT) {
;         const int t = it >> 7, col = (it & 127) * 8, w = 2 << (col >> 8), cnt = (t + 1 < w) ? t + 1 : w;
;         u32x4 v[16];
; #pragma unroll
;         for (int k = 0; k < 16; ++k) v[k] = (k < cnt) ? *(const u32x4*)(Z + (size_t)(t - k) * EVN + col) : (u32x4){0u, 0u, 0u, 0u};
;         float s[8];
; #pragma unroll
;         for (int e = 0; e < 8; ++e) s[e] = 0.f;
; #pragma unroll
;         for (int k = 0; k < 16; ++k) { s[0] += bf_lo(v[k].x); s[1] += bf_hi(v[k].x); s[2] += bf_lo(v[k].y); s[3] += bf_hi(v[k].y); s[4] += bf_lo(v[k].z); s[5] += bf_hi(v[k].z); s[6] += bf_lo(v[k].w); s[7] += bf_hi(v[k].w); }
.LBB0_433:
	s_or_b64 exec, exec, s[8:9]
	s_load_dwordx2 s[4:5], s[0:1], 0xe0
	s_load_dword s20, s[0:1], 0xf8
	v_readfirstlane_b32 s8, v0
	v_mbcnt_lo_u32_b32 v1, -1, 0
	v_mbcnt_hi_u32_b32 v1, -1, v1
	v_and_b32_e32 v2, 31, v1
	v_lshrrev_b32_e32 v3, 5, v1
	s_waitcnt lgkmcnt(0)
	s_lshr_b32 s8, s8, 6
	s_lshl_b32 s9, s18, 3
	s_add_u32 s8, s8, s9
	s_lshl_b32 s20, s20, 3
	s_add_u32 s6, s4, 0x42800000
	s_addc_u32 s7, s5, 0
	s_add_u32 s4, s4, 0x3a800000
	s_addc_u32 s5, s5, 0
.Lpd2_loop:
	s_cmp_ge_u32 s8, 0x800
	s_cbranch_scc1 .Lpd2_done
	s_cmp_lt_u32 s8, 4
	s_cbranch_scc1 .Lpd2_next
	s_and_b32 s9, s8, 3
	s_lshr_b32 s10, s8, 2
	s_lshl_b32 s11, 2, s9
	v_lshl_add_u32 v4, s10, 1, v3
	v_lshlrev_b32_e32 v4, 3, v4
	s_lshl_b32 s12, s9, 5
	v_add_u32_e32 v5, s12, v2
	v_lshlrev_b32_e32 v5, 4, v5
	v_lshl_add_u32 v7, v4, 11, v5
	v_add_u32_e32 v6, 1, v4
	v_subrev_u32_e32 v6, s11, v6
	v_mul_u32_u24_e32 v6, 0x2800, v6
	v_add_u32_e32 v6, v6, v5
	s_mov_b64 s[12:13], s[4:5]
	s_mov_b64 s[14:15], s[6:7]
	s_cmp_eq_u32 s9, 0
	s_cbranch_scc1 .Lpd2_w2
	s_cmp_eq_u32 s9, 1
	s_cbranch_scc1 .Lpd2_w4
	s_cmp_eq_u32 s9, 2
	s_cbranch_scc1 .Lpd2_w8
.Lpd2_w16:
	v_mov_b32_e32 v192, 0x3d800000
	v_mov_b32_e32 v193, 0x3d800000
	global_load_dwordx4 v[10:13], v6, s[12:13]
	s_add_u32 s12, s12, 0x2800
	s_addc_u32 s13, s13, 0
	global_load_dwordx4 v[14:17], v6, s[12:13]
	s_add_u32 s12, s12, 0x2800
	s_addc_u32 s13, s13, 0
	global_load_dwordx4 v[18:21], v6, s[12:13]
	s_add_u32 s12, s12, 0x2800
	s_addc_u32 s13, s13, 0
	global_load_dwordx4 v[22:25], v6, s[12:13]
	s_add_u32 s12, s12, 0x2800
	s_addc_u32 s13, s13, 0
	global_load_dwordx4 v[26:29], v6, s[12:13]
	s_add_u32 s12, s12, 0x2800
	s_addc_u32 s13, s13, 0
	global_load_dwordx4 v[30:33], v6, s[12:13]
	s_add_u32 s12, s12, 0x2800
	s_addc_u32 s13, s13, 0
	global_load_dwordx4 v[34:37], v6, s[12:13]
	s_add_u32 s12, s12, 0x2800
	s_addc_u32 s13, s13, 0
	global_load_dwordx4 v[38:41], v6, s[12:13]
	s_add_u32 s12, s12, 0x2800
	s_addc_u32 s13, s13, 0
	global_load_dwordx4 v[42:45], v6, s[12:13]
	s_add_u32 s12, s12, 0x2800
	s_addc_u32 s13, s13, 0
	global_load_dwordx4 v[46:49], v6, s[12:13]
	s_add_u32 s12, s12, 0x2800
	s_addc_u32 s13, s13, 0
	global_load_dwordx4 v[50:53], v6, s[12:13]
	s_add_u32 s12, s12, 0x2800
	s_addc_u32 s13, s13, 0
	global_load_dwordx4 v[54:57], v6, s[12:13]
	s_add_u32 s12, s12, 0x2800
	s_addc_u32 s13, s13, 0
	global_load_dwordx4 v[58:61], v6, s[12:13]
	s_add_u32 s12, s12, 0x2800
	s_addc_u32 s13, s13, 0
	global_load_dwordx4 v[62:65], v6, s[12:13]
	s_add_u32 s12, s12, 0x2800
	s_addc_u32 s13, s13, 0
	global_load_dwordx4 v[66:69], v6, s[12:13]
	s_add_u32 s12, s12, 0x2800
	s_addc_u32 s13, s13, 0
	global_load_dwordx4 v[70:73], v6, s[12:13]
	s_add_u32 s12, s12, 0x2800
	s_addc_u32 s13, s13, 0
	global_load_dwordx4 v[74:77], v6, s[12:13]
	s_add_u32 s12, s12, 0x2800
	s_addc_u32 s13, s13, 0
	global_load_dwordx4 v[78:81], v6, s[12:13]
	s_add_u32 s12, s12, 0x2800
	s_addc_u32 s13, s13, 0
	global_load_dwordx4 v[82:85], v6, s[12:13]
	s_add_u32 s12, s12, 0x2800
	s_addc_u32 s13, s13, 0
	global_load_dwordx4 v[86:89], v6, s[12:13]
	s_add_u32 s12, s12, 0x2800
	s_addc_u32 s13, s13, 0
	global_load_dwordx4 v[90:93], v6, s[12:13]
	s_add_u32 s12, s12, 0x2800
	s_addc_u32 s13, s13, 0
	global_load_dwordx4 v[94:97], v6, s[12:13]
	s_add_u32 s12, s12, 0x2800
	s_addc_u32 s13, s13, 0
	global_load_dwordx4 v[98:101], v6, s[12:13]
	s_waitcnt vmcnt(22)
	v_lshlrev_b32_e32 v104, 16, v10
	v_and_b32_e32 v105, 0xffff0000, v10
	v_lshlrev_b32_e32 v106, 16, v11
	v_and_b32_e32 v107, 0xffff0000, v11
	v_lshlrev_b32_e32 v108, 16, v12
	v_and_b32_e32 v109, 0xffff0000, v12
	v_lshlrev_b32_e32 v110, 16, v13
	v_and_b32_e32 v111, 0xffff0000, v13
	s_waitcnt vmcnt(21)
	v_lshlrev_b32_e32 v112, 16, v14
	v_and_b32_e32 v113, 0xffff0000, v14
	v_lshlrev_b32_e32 v114, 16, v15
	v_and_b32_e32 v115, 0xffff0000, v15
	v_lshlrev_b32_e32 v116, 16, v16
	v_and_b32_e32 v117, 0xffff0000, v16
	v_lshlrev_b32_e32 v118, 16, v17
	v_and_b32_e32 v119, 0xffff0000, v17
	v_pk_add_f32 v[176:177], v[104:105], v[112:113]
	v_pk_add_f32 v[178:179], v[106:107], v[114:115]
	v_pk_add_f32 v[180:181], v[108:109], v[116:117]
	v_pk_add_f32 v[182:183], v[110:111], v[118:119]
	s_waitcnt vmcnt(20)
	v_lshlrev_b32_e32 v120, 16, v18
	v_and_b32_e32 v121, 0xffff0000, v18
	v_lshlrev_b32_e32 v122, 16, v19
	v_and_b32_e32 v123, 0xffff0000, v19
	v_lshlrev_b32_e32 v124, 16, v20
	v_and_b32_e32 v125, 0xffff0000, v20
	v_lshlrev_b32_e32 v126, 16, v21
	v_and_b32_e32 v127, 0xffff0000, v21
	v_pk_add_f32 v[176:177], v[176:177], v[120:121]
	v_pk_add_f32 v[178:179], v[178:179], v[122:123]
	v_pk_add_f32 v[180:181], v[180:181], v[124:125]
	v_pk_add_f32 v[182:183], v[182:183], v[126:127]
	s_waitcnt vmcnt(19)
	v_lshlrev_b32_e32 v128, 16, v22
	v_and_b32_e32 v129, 0xffff0000, v22
	v_lshlrev_b32_e32 v130, 16, v23
	v_and_b32_e32 v131, 0xffff0000, v23
	v_lshlrev_b32_e32 v132, 16, v24
	v_and_b32_e32 v133, 0xffff0000, v24
	v_lshlrev_b32_e32 v134, 16, v25
	v_and_b32_e32 v135, 0xffff0000, v25
	v_pk_add_f32 v[176:177], v[176:177], v[128:129]
	v_pk_add_f32 v[178:179], v[178:179], v[130:131]
	v_pk_add_f32 v[180:181], v[180:181], v[132:133]
	v_pk_add_f32 v[182:183], v[182:183], v[134:135]
	s_waitcnt vmcnt(18)
	v_lshlrev_b32_e32 v136, 16, v26
	v_and_b32_e32 v137, 0xffff0000, v26
	v_lshlrev_b32_e32 v138, 16, v27
	v_and_b32_e32 v139, 0xffff0000, v27
	v_lshlrev_b32_e32 v140, 16, v28
	v_and_b32_e32 v141, 0xffff0000, v28
	v_lshlrev_b32_e32 v142, 16, v29
	v_and_b32_e32 v143, 0xffff0000, v29
	v_pk_add_f32 v[176:177], v[176:177], v[136:137]
	v_pk_add_f32 v[178:179], v[178:179], v[138:139]
	v_pk_add_f32 v[180:181], v[180:181], v[140:141]
	v_pk_add_f32 v[182:183], v[182:183], v[142:143]
	s_waitcnt vmcnt(17)
; __device__ __forceinline__ unsigned cvt_pk_bf16(float lo, float hi) { unsigned r; asm volatile("v_cvt_pk_bf16_f32 %0, %1, %2" : "=v"(r) : "v"(lo), "v"(hi)); return r; }
; __device__ __forceinline__ void pool_diffs(const bf16_t* Z, bf16_t* DP, int G) {
;     ...
;         for (int k = 0; k < 16; ++k) { s[0] += bf_lo(v[k].x); s[1] += bf_hi(v[k].x); s[2] += bf_lo(v[k].y); s[3] += bf_hi(v[k].y); s[4] += bf_lo(v[k].z); s[5] += bf_hi(v[k].z); s[6] += bf_lo(v[k].w); s[7] += bf_hi(v[k].w); }
;         const float ic = 1.0f / (float)cnt; u32x4 o; const u32x4 c0 = v[0];
;         o.x = cvt_pk_bf16(s[0] * ic - bf_lo(c0.x), s[1] * ic - bf_hi(c0.x)); o.y = cvt_pk_bf16(s[2] * ic - bf_lo(c0.y), s[3] * ic - bf_hi(c0.y));
;         o.z = cvt_pk_bf16(s[4] * ic - bf_lo(c0.z), s[5] * ic - bf_hi(c0.z)); o.w = cvt_pk_bf16(s[6] * ic - bf_lo(c0.w), s[7] * ic - bf_hi(c0.w));
;         *(u32x4*)(DP + (size_t)t * 1024 + col) = o;
	v_lshlrev_b32_e32 v144, 16, v30
	v_and_b32_e32 v145, 0xffff0000, v30
	v_lshlrev_b32_e32 v146, 16, v31
	v_and_b32_e32 v147, 0xffff0000, v31
	v_lshlrev_b32_e32 v148, 16, v32
	v_and_b32_e32 v149, 0xffff0000, v32
	v_lshlrev_b32_e32 v150, 16, v33
	v_and_b32_e32 v151, 0xffff0000, v33
	v_pk_add_f32 v[176:177], v[176:177], v[144:145]
	v_pk_add_f32 v[178:179], v[178:179], v[146:147]
	v_pk_add_f32 v[180:181], v[180:181], v[148:149]
	v_pk_add_f32 v[182:183], v[182:183], v[150:151]
	s_waitcnt vmcnt(16)
	v_lshlrev_b32_e32 v152, 16, v34
	v_and_b32_e32 v153, 0xffff0000, v34
	v_lshlrev_b32_e32 v154, 16, v35
	v_and_b32_e32 v155, 0xffff0000, v35
	v_lshlrev_b32_e32 v156, 16, v36
	v_and_b32_e32 v157, 0xffff0000, v36
	v_lshlrev_b32_e32 v158, 16, v37
	v_and_b32_e32 v159, 0xffff0000, v37
	v_pk_add_f32 v[176:177], v[176:177], v[152:153]
	v_pk_add_f32 v[178:179], v[178:179], v[154:155]
	v_pk_add_f32 v[180:181], v[180:181], v[156:157]
	v_pk_add_f32 v[182:183], v[182:183], v[158:159]
	s_waitcnt vmcnt(15)
	v_lshlrev_b32_e32 v160, 16, v38
	v_and_b32_e32 v161, 0xffff0000, v38
	v_lshlrev_b32_e32 v162, 16, v39
	v_and_b32_e32 v163, 0xffff0000, v39
	v_lshlrev_b32_e32 v164, 16, v40
	v_and_b32_e32 v165, 0xffff0000, v40
	v_lshlrev_b32_e32 v166, 16, v41
	v_and_b32_e32 v167, 0xffff0000, v41
	v_pk_add_f32 v[176:177], v[176:177], v[160:161]
	v_pk_add_f32 v[178:179], v[178:179], v[162:163]
	v_pk_add_f32 v[180:181], v[180:181], v[164:165]
	v_pk_add_f32 v[182:183], v[182:183], v[166:167]
	s_waitcnt vmcnt(14)
	v_lshlrev_b32_e32 v168, 16, v42
	v_and_b32_e32 v169, 0xffff0000, v42
	v_lshlrev_b32_e32 v170, 16, v43
	v_and_b32_e32 v171, 0xffff0000, v43
	v_lshlrev_b32_e32 v172, 16, v44
	v_and_b32_e32 v173, 0xffff0000, v44
	v_lshlrev_b32_e32 v174, 16, v45
	v_and_b32_e32 v175, 0xffff0000, v45
	v_pk_add_f32 v[176:177], v[176:177], v[168:169]
	v_pk_add_f32 v[178:179], v[178:179], v[170:171]
	v_pk_add_f32 v[180:181], v[180:181], v[172:173]
	v_pk_add_f32 v[182:183], v[182:183], v[174:175]
	s_waitcnt vmcnt(13)
	v_lshlrev_b32_e32 v160, 16, v46
	v_and_b32_e32 v161, 0xffff0000, v46
	v_lshlrev_b32_e32 v162, 16, v47
	v_and_b32_e32 v163, 0xffff0000, v47
	v_lshlrev_b32_e32 v164, 16, v48
	v_and_b32_e32 v165, 0xffff0000, v48
	v_lshlrev_b32_e32 v166, 16, v49
	v_and_b32_e32 v167, 0xffff0000, v49
	v_pk_add_f32 v[176:177], v[176:177], v[160:161]
	v_pk_add_f32 v[178:179], v[178:179], v[162:163]
	v_pk_add_f32 v[180:181], v[180:181], v[164:165]
	v_pk_add_f32 v[182:183], v[182:183], v[166:167]
	s_waitcnt vmcnt(12)
	v_lshlrev_b32_e32 v168, 16, v50
	v_and_b32_e32 v169, 0xffff0000, v50
	v_lshlrev_b32_e32 v170, 16, v51
	v_and_b32_e32 v171, 0xffff0000, v51
	v_lshlrev_b32_e32 v172, 16, v52
	v_and_b32_e32 v173, 0xffff0000, v52
	v_lshlrev_b32_e32 v174, 16, v53
	v_and_b32_e32 v175, 0xffff0000, v53
	v_pk_add_f32 v[176:177], v[176:177], v[168:169]
	v_pk_add_f32 v[178:179], v[178:179], v[170:171]
	v_pk_add_f32 v[180:181], v[180:181], v[172:173]
	v_pk_add_f32 v[182:183], v[182:183], v[174:175]
	s_waitcnt vmcnt(11)
	v_lshlrev_b32_e32 v160, 16, v54
	v_and_b32_e32 v161, 0xffff0000, v54
	v_lshlrev_b32_e32 v162, 16, v55
	v_and_b32_e32 v163, 0xffff0000, v55
	v_lshlrev_b32_e32 v164, 16, v56
	v_and_b32_e32 v165, 0xffff0000, v56
	v_lshlrev_b32_e32 v166, 16, v57
	v_and_b32_e32 v167, 0xffff0000, v57
	v_pk_add_f32 v[176:177], v[176:177], v[160:161]
	v_pk_add_f32 v[178:179], v[178:179], v[162:163]
	v_pk_add_f32 v[180:181], v[180:181], v[164:165]
	v_pk_add_f32 v[182:183], v[182:183], v[166:167]
	s_waitcnt vmcnt(10)
	v_lshlrev_b32_e32 v168, 16, v58
	v_and_b32_e32 v169, 0xffff0000, v58
	v_lshlrev_b32_e32 v170, 16, v59
	v_and_b32_e32 v171, 0xffff0000, v59
	v_lshlrev_b32_e32 v172, 16, v60
	v_and_b32_e32 v173, 0xffff0000, v60
	v_lshlrev_b32_e32 v174, 16, v61
	v_and_b32_e32 v175, 0xffff0000, v61
	v_pk_add_f32 v[176:177], v[176:177], v[168:169]
	v_pk_add_f32 v[178:179], v[178:179], v[170:171]
	v_pk_add_f32 v[180:181], v[180:181], v[172:173]
	v_pk_add_f32 v[182:183], v[182:183], v[174:175]
	s_waitcnt vmcnt(9)
	v_lshlrev_b32_e32 v160, 16, v62
	v_and_b32_e32 v161, 0xffff0000, v62
	v_lshlrev_b32_e32 v162, 16, v63
	v_and_b32_e32 v163, 0xffff0000, v63
	v_lshlrev_b32_e32 v164, 16, v64
	v_and_b32_e32 v165, 0xffff0000, v64
	v_lshlrev_b32_e32 v166, 16, v65
	v_and_b32_e32 v167, 0xffff0000, v65
	v_pk_add_f32 v[176:177], v[176:177], v[160:161]
	v_pk_add_f32 v[178:179], v[178:179], v[162:163]
	v_pk_add_f32 v[180:181], v[180:181], v[164:165]
	v_pk_add_f32 v[182:183], v[182:183], v[166:167]
	s_waitcnt vmcnt(8)
	v_lshlrev_b32_e32 v168, 16, v66
	v_and_b32_e32 v169, 0xffff0000, v66
	v_lshlrev_b32_e32 v170, 16, v67
	v_and_b32_e32 v171, 0xffff0000, v67
	v_lshlrev_b32_e32 v172, 16, v68
	v_and_b32_e32 v173, 0xffff0000, v68
	v_lshlrev_b32_e32 v174, 16, v69
	v_and_b32_e32 v175, 0xffff0000, v69
	v_pk_add_f32 v[176:177], v[176:177], v[168:169]
	v_pk_add_f32 v[178:179], v[178:179], v[170:171]
	v_pk_add_f32 v[180:181], v[180:181], v[172:173]
	v_pk_add_f32 v[182:183], v[182:183], v[174:175]
	s_waitcnt vmcnt(7)
	v_lshlrev_b32_e32 v160, 16, v70
	v_and_b32_e32 v161, 0xffff0000, v70
	v_lshlrev_b32_e32 v162, 16, v71
	v_and_b32_e32 v163, 0xffff0000, v71
	v_lshlrev_b32_e32 v164, 16, v72
	v_and_b32_e32 v165, 0xffff0000, v72
	v_lshlrev_b32_e32 v166, 16, v73
	v_and_b32_e32 v167, 0xffff0000, v73
	v_pk_add_f32 v[176:177], v[176:177], v[160:161]
	v_pk_add_f32 v[178:179], v[178:179], v[162:163]
	v_pk_add_f32 v[180:181], v[180:181], v[164:165]
	v_pk_add_f32 v[182:183], v[182:183], v[166:167]
	v_pk_fma_f32 v[194:195], v[176:177], v[192:193], v[160:161] neg_lo:[0,0,1] neg_hi:[0,0,1]
	v_pk_fma_f32 v[196:197], v[178:179], v[192:193], v[162:163] neg_lo:[0,0,1] neg_hi:[0,0,1]
	v_pk_fma_f32 v[198:199], v[180:181], v[192:193], v[164:165] neg_lo:[0,0,1] neg_hi:[0,0,1]
	v_pk_fma_f32 v[200:201], v[182:183], v[192:193], v[166:167] neg_lo:[0,0,1] neg_hi:[0,0,1]
	v_cvt_pk_bf16_f32 v184, v194, v195
	v_cvt_pk_bf16_f32 v185, v196, v197
	v_cvt_pk_bf16_f32 v186, v198, v199
	v_cvt_pk_bf16_f32 v187, v200, v201
	global_store_dwordx4 v7, v[184:187], s[14:15]
	s_add_u32 s14, s14, 0x800
	s_addc_u32 s15, s15, 0
	s_waitcnt vmcnt(7)
; __device__ __forceinline__ unsigned cvt_pk_bf16(float lo, float hi) { unsigned r; asm volatile("v_cvt_pk_bf16_f32 %0, %1, %2" : "=v"(r) : "v"(lo), "v"(hi)); return r; }
; __device__ __forceinline__ void pool_diffs(const bf16_t* Z, bf16_t* DP, int G) {
;     ...
;         for (int k = 0; k < 16; ++k) { s[0] += bf_lo(v[k].x); s[1] += bf_hi(v[k].x); s[2] += bf_lo(v[k].y); s[3] += bf_hi(v[k].y); s[4] += bf_lo(v[k].z); s[5] += bf_hi(v[k].z); s[6] += bf_lo(v[k].w); s[7] += bf_hi(v[k].w); }
;         const float ic = 1.0f / (float)cnt; u32x4 o; const u32x4 c0 = v[0];
;         o.x = cvt_pk_bf16(s[0] * ic - bf_lo(c0.x), s[1] * ic - bf_hi(c0.x)); o.y = cvt_pk_bf16(s[2] * ic - bf_lo(c0.y), s[3] * ic - bf_hi(c0.y));
;         o.z = cvt_pk_bf16(s[4] * ic - bf_lo(c0.z), s[5] * ic - bf_hi(c0.z)); o.w = cvt_pk_bf16(s[6] * ic - bf_lo(c0.w), s[7] * ic - bf_hi(c0.w));
;         *(u32x4*)(DP + (size_t)t * 1024 + col) = o;
	v_lshlrev_b32_e32 v168, 16, v74
	v_and_b32_e32 v169, 0xffff0000, v74
	v_lshlrev_b32_e32 v170, 16, v75
	v_and_b32_e32 v171, 0xffff0000, v75
	v_lshlrev_b32_e32 v172, 16, v76
	v_and_b32_e32 v173, 0xffff0000, v76
	v_lshlrev_b32_e32 v174, 16, v77
	v_and_b32_e32 v175, 0xffff0000, v77
	v_pk_add_f32 v[176:177], v[176:177], v[168:169]
	v_pk_add_f32 v[178:179], v[178:179], v[170:171]
	v_pk_add_f32 v[180:181], v[180:181], v[172:173]
	v_pk_add_f32 v[182:183], v[182:183], v[174:175]
	v_pk_add_f32 v[176:177], v[176:177], v[104:105] neg_lo:[0,1] neg_hi:[0,1]
	v_pk_add_f32 v[178:179], v[178:179], v[106:107] neg_lo:[0,1] neg_hi:[0,1]
	v_pk_add_f32 v[180:181], v[180:181], v[108:109] neg_lo:[0,1] neg_hi:[0,1]
	v_pk_add_f32 v[182:183], v[182:183], v[110:111] neg_lo:[0,1] neg_hi:[0,1]
	v_pk_fma_f32 v[194:195], v[176:177], v[192:193], v[168:169] neg_lo:[0,0,1] neg_hi:[0,0,1]
	v_pk_fma_f32 v[196:197], v[178:179], v[192:193], v[170:171] neg_lo:[0,0,1] neg_hi:[0,0,1]
	v_pk_fma_f32 v[198:199], v[180:181], v[192:193], v[172:173] neg_lo:[0,0,1] neg_hi:[0,0,1]
	v_pk_fma_f32 v[200:201], v[182:183], v[192:193], v[174:175] neg_lo:[0,0,1] neg_hi:[0,0,1]
	v_cvt_pk_bf16_f32 v188, v194, v195
	v_cvt_pk_bf16_f32 v189, v196, v197
	v_cvt_pk_bf16_f32 v190, v198, v199
	v_cvt_pk_bf16_f32 v191, v200, v201
	global_store_dwordx4 v7, v[188:191], s[14:15]
	s_add_u32 s14, s14, 0x800
	s_addc_u32 s15, s15, 0
	s_waitcnt vmcnt(7)
	v_lshlrev_b32_e32 v160, 16, v78
	v_and_b32_e32 v161, 0xffff0000, v78
	v_lshlrev_b32_e32 v162, 16, v79
	v_and_b32_e32 v163, 0xffff0000, v79
	v_lshlrev_b32_e32 v164, 16, v80
	v_and_b32_e32 v165, 0xffff0000, v80
	v_lshlrev_b32_e32 v166, 16, v81
	v_and_b32_e32 v167, 0xffff0000, v81
	v_pk_add_f32 v[176:177], v[176:177], v[160:161]
	v_pk_add_f32 v[178:179], v[178:179], v[162:163]
	v_pk_add_f32 v[180:181], v[180:181], v[164:165]
	v_pk_add_f32 v[182:183], v[182:183], v[166:167]
	v_pk_add_f32 v[176:177], v[176:177], v[112:113] neg_lo:[0,1] neg_hi:[0,1]
	v_pk_add_f32 v[178:179], v[178:179], v[114:115] neg_lo:[0,1] neg_hi:[0,1]
	v_pk_add_f32 v[180:181], v[180:181], v[116:117] neg_lo:[0,1] neg_hi:[0,1]
	v_pk_add_f32 v[182:183], v[182:183], v[118:119] neg_lo:[0,1] neg_hi:[0,1]
	v_pk_fma_f32 v[194:195], v[176:177], v[192:193], v[160:161] neg_lo:[0,0,1] neg_hi:[0,0,1]
	v_pk_fma_f32 v[196:197], v[178:179], v[192:193], v[162:163] neg_lo:[0,0,1] neg_hi:[0,0,1]
	v_pk_fma_f32 v[198:199], v[180:181], v[192:193], v[164:165] neg_lo:[0,0,1] neg_hi:[0,0,1]
	v_pk_fma_f32 v[200:201], v[182:183], v[192:193], v[166:167] neg_lo:[0,0,1] neg_hi:[0,0,1]
	v_cvt_pk_bf16_f32 v184, v194, v195
	v_cvt_pk_bf16_f32 v185, v196, v197
	v_cvt_pk_bf16_f32 v186, v198, v199
	v_cvt_pk_bf16_f32 v187, v200, v201
	global_store_dwordx4 v7, v[184:187], s[14:15]
	s_add_u32 s14, s14, 0x800
	s_addc_u32 s15, s15, 0
	s_waitcnt vmcnt(7)
	v_lshlrev_b32_e32 v168, 16, v82
	v_and_b32_e32 v169, 0xffff0000, v82
	v_lshlrev_b32_e32 v170, 16, v83
	v_and_b32_e32 v171, 0xffff0000, v83
	v_lshlrev_b32_e32 v172, 16, v84
	v_and_b32_e32 v173, 0xffff0000, v84
	v_lshlrev_b32_e32 v174, 16, v85
	v_and_b32_e32 v175, 0xffff0000, v85
	v_pk_add_f32 v[176:177], v[176:177], v[168:169]
	v_pk_add_f32 v[178:179], v[178:179], v[170:171]
	v_pk_add_f32 v[180:181], v[180:181], v[172:173]
	v_pk_add_f32 v[182:183], v[182:183], v[174:175]
	v_pk_add_f32 v[176:177], v[176:177], v[120:121] neg_lo:[0,1] neg_hi:[0,1]
	v_pk_add_f32 v[178:179], v[178:179], v[122:123] neg_lo:[0,1] neg_hi:[0,1]
	v_pk_add_f32 v[180:181], v[180:181], v[124:125] neg_lo:[0,1] neg_hi:[0,1]
	v_pk_add_f32 v[182:183], v[182:183], v[126:127] neg_lo:[0,1] neg_hi:[0,1]
	v_pk_fma_f32 v[194:195], v[176:177], v[192:193], v[168:169] neg_lo:[0,0,1] neg_hi:[0,0,1]
	v_pk_fma_f32 v[196:197], v[178:179], v[192:193], v[170:171] neg_lo:[0,0,1] neg_hi:[0,0,1]
	v_pk_fma_f32 v[198:199], v[180:181], v[192:193], v[172:173] neg_lo:[0,0,1] neg_hi:[0,0,1]
	v_pk_fma_f32 v[200:201], v[182:183], v[192:193], v[174:175] neg_lo:[0,0,1] neg_hi:[0,0,1]
	v_cvt_pk_bf16_f32 v188, v194, v195
	v_cvt_pk_bf16_f32 v189, v196, v197
	v_cvt_pk_bf16_f32 v190, v198, v199
	v_cvt_pk_bf16_f32 v191, v200, v201
	global_store_dwordx4 v7, v[188:191], s[14:15]
	s_add_u32 s14, s14, 0x800
	s_addc_u32 s15, s15, 0
	s_waitcnt vmcnt(7)
	v_lshlrev_b32_e32 v160, 16, v86
	v_and_b32_e32 v161, 0xffff0000, v86
	v_lshlrev_b32_e32 v162, 16, v87
	v_and_b32_e32 v163, 0xffff0000, v87
	v_lshlrev_b32_e32 v164, 16, v88
	v_and_b32_e32 v165, 0xffff0000, v88
	v_lshlrev_b32_e32 v166, 16, v89
	v_and_b32_e32 v167, 0xffff0000, v89
	v_pk_add_f32 v[176:177], v[176:177], v[160:161]
	v_pk_add_f32 v[178:179], v[178:179], v[162:163]
	v_pk_add_f32 v[180:181], v[180:181], v[164:165]
	v_pk_add_f32 v[182:183], v[182:183], v[166:167]
	v_pk_add_f32 v[176:177], v[176:177], v[128:129] neg_lo:[0,1] neg_hi:[0,1]
	v_pk_add_f32 v[178:179], v[178:179], v[130:131] neg_lo:[0,1] neg_hi:[0,1]
	v_pk_add_f32 v[180:181], v[180:181], v[132:133] neg_lo:[0,1] neg_hi:[0,1]
	v_pk_add_f32 v[182:183], v[182:183], v[134:135] neg_lo:[0,1] neg_hi:[0,1]
	v_pk_fma_f32 v[194:195], v[176:177], v[192:193], v[160:161] neg_lo:[0,0,1] neg_hi:[0,0,1]
	v_pk_fma_f32 v[196:197], v[178:179], v[192:193], v[162:163] neg_lo:[0,0,1] neg_hi:[0,0,1]
	v_pk_fma_f32 v[198:199], v[180:181], v[192:193], v[164:165] neg_lo:[0,0,1] neg_hi:[0,0,1]
	v_pk_fma_f32 v[200:201], v[182:183], v[192:193], v[166:167] neg_lo:[0,0,1] neg_hi:[0,0,1]
	v_cvt_pk_bf16_f32 v184, v194, v195
	v_cvt_pk_bf16_f32 v185, v196, v197
	v_cvt_pk_bf16_f32 v186, v198, v199
	v_cvt_pk_bf16_f32 v187, v200, v201
	global_store_dwordx4 v7, v[184:187], s[14:15]
	s_add_u32 s14, s14, 0x800
	s_addc_u32 s15, s15, 0
	s_waitcnt vmcnt(7)
; __device__ __forceinline__ unsigned cvt_pk_bf16(float lo, float hi) { unsigned r; asm volatile("v_cvt_pk_bf16_f32 %0, %1, %2" : "=v"(r) : "v"(lo), "v"(hi)); return r; }
; __device__ __forceinline__ void pool_diffs(const bf16_t* Z, bf16_t* DP, int G) {
;     ...
;         for (int k = 0; k < 16; ++k) { s[0] += bf_lo(v[k].x); s[1] += bf_hi(v[k].x); s[2] += bf_lo(v[k].y); s[3] += bf_hi(v[k].y); s[4] += bf_lo(v[k].z); s[5] += bf_hi(v[k].z); s[6] += bf_lo(v[k].w); s[7] += bf_hi(v[k].w); }
;         const float ic = 1.0f / (float)cnt; u32x4 o; const u32x4 c0 = v[0];
;         o.x = cvt_pk_bf16(s[0] * ic - bf_lo(c0.x), s[1] * ic - bf_hi(c0.x)); o.y = cvt_pk_bf16(s[2] * ic - bf_lo(c0.y), s[3] * ic - bf_hi(c0.y));
;         o.z = cvt_pk_bf16(s[4] * ic - bf_lo(c0.z), s[5] * ic - bf_hi(c0.z)); o.w = cvt_pk_bf16(s[6] * ic - bf_lo(c0.w), s[7] * ic - bf_hi(c0.w));
;         *(u32x4*)(DP + (size_t)t * 1024 + col) = o;
	v_lshlrev_b32_e32 v168, 16, v90
	v_and_b32_e32 v169, 0xffff0000, v90
	v_lshlrev_b32_e32 v170, 16, v91
	v_and_b32_e32 v171, 0xffff0000, v91
	v_lshlrev_b32_e32 v172, 16, v92
	v_and_b32_e32 v173, 0xffff0000, v92
	v_lshlrev_b32_e32 v174, 16, v93
	v_and_b32_e32 v175, 0xffff0000, v93
	v_pk_add_f32 v[176:177], v[176:177], v[168:169]
	v_pk_add_f32 v[178:179], v[178:179], v[170:171]
	v_pk_add_f32 v[180:181], v[180:181], v[172:173]
	v_pk_add_f32 v[182:183], v[182:183], v[174:175]
	v_pk_add_f32 v[176:177], v[176:177], v[136:137] neg_lo:[0,1] neg_hi:[0,1]
	v_pk_add_f32 v[178:179], v[178:179], v[138:139] neg_lo:[0,1] neg_hi:[0,1]
	v_pk_add_f32 v[180:181], v[180:181], v[140:141] neg_lo:[0,1] neg_hi:[0,1]
	v_pk_add_f32 v[182:183], v[182:183], v[142:143] neg_lo:[0,1] neg_hi:[0,1]
	v_pk_fma_f32 v[194:195], v[176:177], v[192:193], v[168:169] neg_lo:[0,0,1] neg_hi:[0,0,1]
	v_pk_fma_f32 v[196:197], v[178:179], v[192:193], v[170:171] neg_lo:[0,0,1] neg_hi:[0,0,1]
	v_pk_fma_f32 v[198:199], v[180:181], v[192:193], v[172:173] neg_lo:[0,0,1] neg_hi:[0,0,1]
	v_pk_fma_f32 v[200:201], v[182:183], v[192:193], v[174:175] neg_lo:[0,0,1] neg_hi:[0,0,1]
	v_cvt_pk_bf16_f32 v188, v194, v195
	v_cvt_pk_bf16_f32 v189, v196, v197
	v_cvt_pk_bf16_f32 v190, v198, v199
	v_cvt_pk_bf16_f32 v191, v200, v201
	global_store_dwordx4 v7, v[188:191], s[14:15]
	s_add_u32 s14, s14, 0x800
	s_addc_u32 s15, s15, 0
	s_waitcnt vmcnt(7)
	v_lshlrev_b32_e32 v160, 16, v94
	v_and_b32_e32 v161, 0xffff0000, v94
	v_lshlrev_b32_e32 v162, 16, v95
	v_and_b32_e32 v163, 0xffff0000, v95
	v_lshlrev_b32_e32 v164, 16, v96
	v_and_b32_e32 v165, 0xffff0000, v96
	v_lshlrev_b32_e32 v166, 16, v97
	v_and_b32_e32 v167, 0xffff0000, v97
	v_pk_add_f32 v[176:177], v[176:177], v[160:161]
	v_pk_add_f32 v[178:179], v[178:179], v[162:163]
	v_pk_add_f32 v[180:181], v[180:181], v[164:165]
	v_pk_add_f32 v[182:183], v[182:183], v[166:167]
	v_pk_add_f32 v[176:177], v[176:177], v[144:145] neg_lo:[0,1] neg_hi:[0,1]
	v_pk_add_f32 v[178:179], v[178:179], v[146:147] neg_lo:[0,1] neg_hi:[0,1]
	v_pk_add_f32 v[180:181], v[180:181], v[148:149] neg_lo:[0,1] neg_hi:[0,1]
	v_pk_add_f32 v[182:183], v[182:183], v[150:151] neg_lo:[0,1] neg_hi:[0,1]
	v_pk_fma_f32 v[194:195], v[176:177], v[192:193], v[160:161] neg_lo:[0,0,1] neg_hi:[0,0,1]
	v_pk_fma_f32 v[196:197], v[178:179], v[192:193], v[162:163] neg_lo:[0,0,1] neg_hi:[0,0,1]
	v_pk_fma_f32 v[198:199], v[180:181], v[192:193], v[164:165] neg_lo:[0,0,1] neg_hi:[0,0,1]
	v_pk_fma_f32 v[200:201], v[182:183], v[192:193], v[166:167] neg_lo:[0,0,1] neg_hi:[0,0,1]
	v_cvt_pk_bf16_f32 v184, v194, v195
	v_cvt_pk_bf16_f32 v185, v196, v197
	v_cvt_pk_bf16_f32 v186, v198, v199
	v_cvt_pk_bf16_f32 v187, v200, v201
	global_store_dwordx4 v7, v[184:187], s[14:15]
	s_add_u32 s14, s14, 0x800
	s_addc_u32 s15, s15, 0
	s_waitcnt vmcnt(7)
	v_lshlrev_b32_e32 v168, 16, v98
	v_and_b32_e32 v169, 0xffff0000, v98
	v_lshlrev_b32_e32 v170, 16, v99
	v_and_b32_e32 v171, 0xffff0000, v99
	v_lshlrev_b32_e32 v172, 16, v100
	v_and_b32_e32 v173, 0xffff0000, v100
	v_lshlrev_b32_e32 v174, 16, v101
	v_and_b32_e32 v175, 0xffff0000, v101
	v_pk_add_f32 v[176:177], v[176:177], v[168:169]
	v_pk_add_f32 v[178:179], v[178:179], v[170:171]
	v_pk_add_f32 v[180:181], v[180:181], v[172:173]
	v_pk_add_f32 v[182:183], v[182:183], v[174:175]
	v_pk_add_f32 v[176:177], v[176:177], v[152:153] neg_lo:[0,1] neg_hi:[0,1]
	v_pk_add_f32 v[178:179], v[178:179], v[154:155] neg_lo:[0,1] neg_hi:[0,1]
	v_pk_add_f32 v[180:181], v[180:181], v[156:157] neg_lo:[0,1] neg_hi:[0,1]
	v_pk_add_f32 v[182:183], v[182:183], v[158:159] neg_lo:[0,1] neg_hi:[0,1]
	v_pk_fma_f32 v[194:195], v[176:177], v[192:193], v[168:169] neg_lo:[0,0,1] neg_hi:[0,0,1]
	v_pk_fma_f32 v[196:197], v[178:179], v[192:193], v[170:171] neg_lo:[0,0,1] neg_hi:[0,0,1]
	v_pk_fma_f32 v[198:199], v[180:181], v[192:193], v[172:173] neg_lo:[0,0,1] neg_hi:[0,0,1]
	v_pk_fma_f32 v[200:201], v[182:183], v[192:193], v[174:175] neg_lo:[0,0,1] neg_hi:[0,0,1]
	v_cvt_pk_bf16_f32 v188, v194, v195
	v_cvt_pk_bf16_f32 v189, v196, v197
	v_cvt_pk_bf16_f32 v190, v198, v199
	v_cvt_pk_bf16_f32 v191, v200, v201
	global_store_dwordx4 v7, v[188:191], s[14:15]
	s_branch .Lpd2_next
.Lpd2_w8:
	v_mov_b32_e32 v192, 0x3e000000
	v_mov_b32_e32 v193, 0x3e000000
	global_load_dwordx4 v[10:13], v6, s[12:13]
	s_add_u32 s12, s12, 0x2800
	s_addc_u32 s13, s13, 0
	global_load_dwordx4 v[14:17], v6, s[12:13]
	s_add_u32 s12, s12, 0x2800
	s_addc_u32 s13, s13, 0
	global_load_dwordx4 v[18:21], v6, s[12:13]
	s_add_u32 s12, s12, 0x2800
	s_addc_u32 s13, s13, 0
	global_load_dwordx4 v[22:25], v6, s[12:13]
	s_add_u32 s12, s12, 0x2800
	s_addc_u32 s13, s13, 0
	global_load_dwordx4 v[26:29], v6, s[12:13]
	s_add_u32 s12, s12, 0x2800
	s_addc_u32 s13, s13, 0
	global_load_dwordx4 v[30:33], v6, s[12:13]
	s_add_u32 s12, s12, 0x2800
	s_addc_u32 s13, s13, 0
	global_load_dwordx4 v[34:37], v6, s[12:13]
	s_add_u32 s12, s12, 0x2800
	s_addc_u32 s13, s13, 0
	global_load_dwordx4 v[38:41], v6, s[12:13]
	s_add_u32 s12, s12, 0x2800
	s_addc_u32 s13, s13, 0
	global_load_dwordx4 v[42:45], v6, s[12:13]
	s_add_u32 s12, s12, 0x2800
	s_addc_u32 s13, s13, 0
	global_load_dwordx4 v[46:49], v6, s[12:13]
	s_add_u32 s12, s12, 0x2800
	s_addc_u32 s13, s13, 0
	global_load_dwordx4 v[50:53], v6, s[12:13]
	s_add_u32 s12, s12, 0x2800
	s_addc_u32 s13, s13, 0
	global_load_dwordx4 v[54:57], v6, s[12:13]
	s_add_u32 s12, s12, 0x2800
	s_addc_u32 s13, s13, 0
	global_load_dwordx4 v[58:61], v6, s[12:13]
	s_add_u32 s12, s12, 0x2800
	s_addc_u32 s13, s13, 0
	global_load_dwordx4 v[62:65], v6, s[12:13]
	s_add_u32 s12, s12, 0x2800
	s_addc_u32 s13, s13, 0
	global_load_dwordx4 v[66:69], v6, s[12:13]
	s_waitcnt vmcnt(14)
; __device__ __forceinline__ unsigned cvt_pk_bf16(float lo, float hi) { unsigned r; asm volatile("v_cvt_pk_bf16_f32 %0, %1, %2" : "=v"(r) : "v"(lo), "v"(hi)); return r; }
; __device__ __forceinline__ void pool_diffs(const bf16_t* Z, bf16_t* DP, int G) {
;     ...
;         for (int k = 0; k < 16; ++k) { s[0] += bf_lo(v[k].x); s[1] += bf_hi(v[k].x); s[2] += bf_lo(v[k].y); s[3] += bf_hi(v[k].y); s[4] += bf_lo(v[k].z); s[5] += bf_hi(v[k].z); s[6] += bf_lo(v[k].w); s[7] += bf_hi(v[k].w); }
;         const float ic = 1.0f / (float)cnt; u32x4 o; const u32x4 c0 = v[0];
;         o.x = cvt_pk_bf16(s[0] * ic - bf_lo(c0.x), s[1] * ic - bf_hi(c0.x)); o.y = cvt_pk_bf16(s[2] * ic - bf_lo(c0.y), s[3] * ic - bf_hi(c0.y));
;         o.z = cvt_pk_bf16(s[4] * ic - bf_lo(c0.z), s[5] * ic - bf_hi(c0.z)); o.w = cvt_pk_bf16(s[6] * ic - bf_lo(c0.w), s[7] * ic - bf_hi(c0.w));
;         *(u32x4*)(DP + (size_t)t * 1024 + col) = o;
	v_lshlrev_b32_e32 v104, 16, v10
	v_and_b32_e32 v105, 0xffff0000, v10
	v_lshlrev_b32_e32 v106, 16, v11
	v_and_b32_e32 v107, 0xffff0000, v11
	v_lshlrev_b32_e32 v108, 16, v12
	v_and_b32_e32 v109, 0xffff0000, v12
	v_lshlrev_b32_e32 v110, 16, v13
	v_and_b32_e32 v111, 0xffff0000, v13
	s_waitcnt vmcnt(13)
	v_lshlrev_b32_e32 v112, 16, v14
	v_and_b32_e32 v113, 0xffff0000, v14
	v_lshlrev_b32_e32 v114, 16, v15
	v_and_b32_e32 v115, 0xffff0000, v15
	v_lshlrev_b32_e32 v116, 16, v16
	v_and_b32_e32 v117, 0xffff0000, v16
	v_lshlrev_b32_e32 v118, 16, v17
	v_and_b32_e32 v119, 0xffff0000, v17
	v_pk_add_f32 v[176:177], v[104:105], v[112:113]
	v_pk_add_f32 v[178:179], v[106:107], v[114:115]
	v_pk_add_f32 v[180:181], v[108:109], v[116:117]
	v_pk_add_f32 v[182:183], v[110:111], v[118:119]
	s_waitcnt vmcnt(12)
	v_lshlrev_b32_e32 v120, 16, v18
	v_and_b32_e32 v121, 0xffff0000, v18
	v_lshlrev_b32_e32 v122, 16, v19
	v_and_b32_e32 v123, 0xffff0000, v19
	v_lshlrev_b32_e32 v124, 16, v20
	v_and_b32_e32 v125, 0xffff0000, v20
	v_lshlrev_b32_e32 v126, 16, v21
	v_and_b32_e32 v127, 0xffff0000, v21
	v_pk_add_f32 v[176:177], v[176:177], v[120:121]
	v_pk_add_f32 v[178:179], v[178:179], v[122:123]
	v_pk_add_f32 v[180:181], v[180:181], v[124:125]
	v_pk_add_f32 v[182:183], v[182:183], v[126:127]
	s_waitcnt vmcnt(11)
	v_lshlrev_b32_e32 v128, 16, v22
	v_and_b32_e32 v129, 0xffff0000, v22
	v_lshlrev_b32_e32 v130, 16, v23
	v_and_b32_e32 v131, 0xffff0000, v23
	v_lshlrev_b32_e32 v132, 16, v24
	v_and_b32_e32 v133, 0xffff0000, v24
	v_lshlrev_b32_e32 v134, 16, v25
	v_and_b32_e32 v135, 0xffff0000, v25
	v_pk_add_f32 v[176:177], v[176:177], v[128:129]
	v_pk_add_f32 v[178:179], v[178:179], v[130:131]
	v_pk_add_f32 v[180:181], v[180:181], v[132:133]
	v_pk_add_f32 v[182:183], v[182:183], v[134:135]
	s_waitcnt vmcnt(10)
	v_lshlrev_b32_e32 v136, 16, v26
	v_and_b32_e32 v137, 0xffff0000, v26
	v_lshlrev_b32_e32 v138, 16, v27
	v_and_b32_e32 v139, 0xffff0000, v27
	v_lshlrev_b32_e32 v140, 16, v28
	v_and_b32_e32 v141, 0xffff0000, v28
	v_lshlrev_b32_e32 v142, 16, v29
	v_and_b32_e32 v143, 0xffff0000, v29
	v_pk_add_f32 v[176:177], v[176:177], v[136:137]
	v_pk_add_f32 v[178:179], v[178:179], v[138:139]
	v_pk_add_f32 v[180:181], v[180:181], v[140:141]
	v_pk_add_f32 v[182:183], v[182:183], v[142:143]
	s_waitcnt vmcnt(9)
	v_lshlrev_b32_e32 v144, 16, v30
	v_and_b32_e32 v145, 0xffff0000, v30
	v_lshlrev_b32_e32 v146, 16, v31
	v_and_b32_e32 v147, 0xffff0000, v31
	v_lshlrev_b32_e32 v148, 16, v32
	v_and_b32_e32 v149, 0xffff0000, v32
	v_lshlrev_b32_e32 v150, 16, v33
	v_and_b32_e32 v151, 0xffff0000, v33
	v_pk_add_f32 v[176:177], v[176:177], v[144:145]
	v_pk_add_f32 v[178:179], v[178:179], v[146:147]
	v_pk_add_f32 v[180:181], v[180:181], v[148:149]
	v_pk_add_f32 v[182:183], v[182:183], v[150:151]
	s_waitcnt vmcnt(8)
	v_lshlrev_b32_e32 v152, 16, v34
	v_and_b32_e32 v153, 0xffff0000, v34
	v_lshlrev_b32_e32 v154, 16, v35
	v_and_b32_e32 v155, 0xffff0000, v35
	v_lshlrev_b32_e32 v156, 16, v36
	v_and_b32_e32 v157, 0xffff0000, v36
	v_lshlrev_b32_e32 v158, 16, v37
	v_and_b32_e32 v159, 0xffff0000, v37
	v_pk_add_f32 v[176:177], v[176:177], v[152:153]
	v_pk_add_f32 v[178:179], v[178:179], v[154:155]
	v_pk_add_f32 v[180:181], v[180:181], v[156:157]
	v_pk_add_f32 v[182:183], v[182:183], v[158:159]
	s_waitcnt vmcnt(7)
	v_lshlrev_b32_e32 v160, 16, v38
	v_and_b32_e32 v161, 0xffff0000, v38
	v_lshlrev_b32_e32 v162, 16, v39
	v_and_b32_e32 v163, 0xffff0000, v39
	v_lshlrev_b32_e32 v164, 16, v40
	v_and_b32_e32 v165, 0xffff0000, v40
	v_lshlrev_b32_e32 v166, 16, v41
	v_and_b32_e32 v167, 0xffff0000, v41
	v_pk_add_f32 v[176:177], v[176:177], v[160:161]
	v_pk_add_f32 v[178:179], v[178:179], v[162:163]
	v_pk_add_f32 v[180:181], v[180:181], v[164:165]
	v_pk_add_f32 v[182:183], v[182:183], v[166:167]
	v_pk_fma_f32 v[194:195], v[176:177], v[192:193], v[160:161] neg_lo:[0,0,1] neg_hi:[0,0,1]
	v_pk_fma_f32 v[196:197], v[178:179], v[192:193], v[162:163] neg_lo:[0,0,1] neg_hi:[0,0,1]
	v_pk_fma_f32 v[198:199], v[180:181], v[192:193], v[164:165] neg_lo:[0,0,1] neg_hi:[0,0,1]
	v_pk_fma_f32 v[200:201], v[182:183], v[192:193], v[166:167] neg_lo:[0,0,1] neg_hi:[0,0,1]
	v_cvt_pk_bf16_f32 v184, v194, v195
	v_cvt_pk_bf16_f32 v185, v196, v197
	v_cvt_pk_bf16_f32 v186, v198, v199
	v_cvt_pk_bf16_f32 v187, v200, v201
	global_store_dwordx4 v7, v[184:187], s[14:15]
	s_add_u32 s14, s14, 0x800
	s_addc_u32 s15, s15, 0
	s_waitcnt vmcnt(7)
	v_lshlrev_b32_e32 v168, 16, v42
	v_and_b32_e32 v169, 0xffff0000, v42
	v_lshlrev_b32_e32 v170, 16, v43
	v_and_b32_e32 v171, 0xffff0000, v43
	v_lshlrev_b32_e32 v172, 16, v44
	v_and_b32_e32 v173, 0xffff0000, v44
	v_lshlrev_b32_e32 v174, 16, v45
	v_and_b32_e32 v175, 0xffff0000, v45
	v_pk_add_f32 v[176:177], v[176:177], v[168:169]
	v_pk_add_f32 v[178:179], v[178:179], v[170:171]
	v_pk_add_f32 v[180:181], v[180:181], v[172:173]
	v_pk_add_f32 v[182:183], v[182:183], v[174:175]
	v_pk_add_f32 v[176:177], v[176:177], v[104:105] neg_lo:[0,1] neg_hi:[0,1]
	v_pk_add_f32 v[178:179], v[178:179], v[106:107] neg_lo:[0,1] neg_hi:[0,1]
	v_pk_add_f32 v[180:181], v[180:181], v[108:109] neg_lo:[0,1] neg_hi:[0,1]
	v_pk_add_f32 v[182:183], v[182:183], v[110:111] neg_lo:[0,1] neg_hi:[0,1]
	v_pk_fma_f32 v[194:195], v[176:177], v[192:193], v[168:169] neg_lo:[0,0,1] neg_hi:[0,0,1]
	v_pk_fma_f32 v[196:197], v[178:179], v[192:193], v[170:171] neg_lo:[0,0,1] neg_hi:[0,0,1]
	v_pk_fma_f32 v[198:199], v[180:181], v[192:193], v[172:173] neg_lo:[0,0,1] neg_hi:[0,0,1]
	v_pk_fma_f32 v[200:201], v[182:183], v[192:193], v[174:175] neg_lo:[0,0,1] neg_hi:[0,0,1]
	v_cvt_pk_bf16_f32 v188, v194, v195
	v_cvt_pk_bf16_f32 v189, v196, v197
	v_cvt_pk_bf16_f32 v190, v198, v199
	v_cvt_pk_bf16_f32 v191, v200, v201
	global_store_dwordx4 v7, v[188:191], s[14:15]
	s_add_u32 s14, s14, 0x800
	s_addc_u32 s15, s15, 0
	s_waitcnt vmcnt(7)
; __device__ __forceinline__ unsigned cvt_pk_bf16(float lo, float hi) { unsigned r; asm volatile("v_cvt_pk_bf16_f32 %0, %1, %2" : "=v"(r) : "v"(lo), "v"(hi)); return r; }
; __device__ __forceinline__ void pool_diffs(const bf16_t* Z, bf16_t* DP, int G) {
;     ...
;         for (int k = 0; k < 16; ++k) { s[0] += bf_lo(v[k].x); s[1] += bf_hi(v[k].x); s[2] += bf_lo(v[k].y); s[3] += bf_hi(v[k].y); s[4] += bf_lo(v[k].z); s[5] += bf_hi(v[k].z); s[6] += bf_lo(v[k].w); s[7] += bf_hi(v[k].w); }
;         const float ic = 1.0f / (float)cnt; u32x4 o; const u32x4 c0 = v[0];
;         o.x = cvt_pk_bf16(s[0] * ic - bf_lo(c0.x), s[1] * ic - bf_hi(c0.x)); o.y = cvt_pk_bf16(s[2] * ic - bf_lo(c0.y), s[3] * ic - bf_hi(c0.y));
;         o.z = cvt_pk_bf16(s[4] * ic - bf_lo(c0.z), s[5] * ic - bf_hi(c0.z)); o.w = cvt_pk_bf16(s[6] * ic - bf_lo(c0.w), s[7] * ic - bf_hi(c0.w));
;         *(u32x4*)(DP + (size_t)t * 1024 + col) = o;
	v_lshlrev_b32_e32 v160, 16, v46
	v_and_b32_e32 v161, 0xffff0000, v46
	v_lshlrev_b32_e32 v162, 16, v47
	v_and_b32_e32 v163, 0xffff0000, v47
	v_lshlrev_b32_e32 v164, 16, v48
	v_and_b32_e32 v165, 0xffff0000, v48
	v_lshlrev_b32_e32 v166, 16, v49
	v_and_b32_e32 v167, 0xffff0000, v49
	v_pk_add_f32 v[176:177], v[176:177], v[160:161]
	v_pk_add_f32 v[178:179], v[178:179], v[162:163]
	v_pk_add_f32 v[180:181], v[180:181], v[164:165]
	v_pk_add_f32 v[182:183], v[182:183], v[166:167]
	v_pk_add_f32 v[176:177], v[176:177], v[112:113] neg_lo:[0,1] neg_hi:[0,1]
	v_pk_add_f32 v[178:179], v[178:179], v[114:115] neg_lo:[0,1] neg_hi:[0,1]
	v_pk_add_f32 v[180:181], v[180:181], v[116:117] neg_lo:[0,1] neg_hi:[0,1]
	v_pk_add_f32 v[182:183], v[182:183], v[118:119] neg_lo:[0,1] neg_hi:[0,1]
	v_pk_fma_f32 v[194:195], v[176:177], v[192:193], v[160:161] neg_lo:[0,0,1] neg_hi:[0,0,1]
	v_pk_fma_f32 v[196:197], v[178:179], v[192:193], v[162:163] neg_lo:[0,0,1] neg_hi:[0,0,1]
	v_pk_fma_f32 v[198:199], v[180:181], v[192:193], v[164:165] neg_lo:[0,0,1] neg_hi:[0,0,1]
	v_pk_fma_f32 v[200:201], v[182:183], v[192:193], v[166:167] neg_lo:[0,0,1] neg_hi:[0,0,1]
	v_cvt_pk_bf16_f32 v184, v194, v195
	v_cvt_pk_bf16_f32 v185, v196, v197
	v_cvt_pk_bf16_f32 v186, v198, v199
	v_cvt_pk_bf16_f32 v187, v200, v201
	global_store_dwordx4 v7, v[184:187], s[14:15]
	s_add_u32 s14, s14, 0x800
	s_addc_u32 s15, s15, 0
	s_waitcnt vmcnt(7)
	v_lshlrev_b32_e32 v168, 16, v50
	v_and_b32_e32 v169, 0xffff0000, v50
	v_lshlrev_b32_e32 v170, 16, v51
	v_and_b32_e32 v171, 0xffff0000, v51
	v_lshlrev_b32_e32 v172, 16, v52
	v_and_b32_e32 v173, 0xffff0000, v52
	v_lshlrev_b32_e32 v174, 16, v53
	v_and_b32_e32 v175, 0xffff0000, v53
	v_pk_add_f32 v[176:177], v[176:177], v[168:169]
	v_pk_add_f32 v[178:179], v[178:179], v[170:171]
	v_pk_add_f32 v[180:181], v[180:181], v[172:173]
	v_pk_add_f32 v[182:183], v[182:183], v[174:175]
	v_pk_add_f32 v[176:177], v[176:177], v[120:121] neg_lo:[0,1] neg_hi:[0,1]
	v_pk_add_f32 v[178:179], v[178:179], v[122:123] neg_lo:[0,1] neg_hi:[0,1]
	v_pk_add_f32 v[180:181], v[180:181], v[124:125] neg_lo:[0,1] neg_hi:[0,1]
	v_pk_add_f32 v[182:183], v[182:183], v[126:127] neg_lo:[0,1] neg_hi:[0,1]
	v_pk_fma_f32 v[194:195], v[176:177], v[192:193], v[168:169] neg_lo:[0,0,1] neg_hi:[0,0,1]
	v_pk_fma_f32 v[196:197], v[178:179], v[192:193], v[170:171] neg_lo:[0,0,1] neg_hi:[0,0,1]
	v_pk_fma_f32 v[198:199], v[180:181], v[192:193], v[172:173] neg_lo:[0,0,1] neg_hi:[0,0,1]
	v_pk_fma_f32 v[200:201], v[182:183], v[192:193], v[174:175] neg_lo:[0,0,1] neg_hi:[0,0,1]
	v_cvt_pk_bf16_f32 v188, v194, v195
	v_cvt_pk_bf16_f32 v189, v196, v197
	v_cvt_pk_bf16_f32 v190, v198, v199
	v_cvt_pk_bf16_f32 v191, v200, v201
	global_store_dwordx4 v7, v[188:191], s[14:15]
	s_add_u32 s14, s14, 0x800
	s_addc_u32 s15, s15, 0
	s_waitcnt vmcnt(7)
	v_lshlrev_b32_e32 v160, 16, v54
	v_and_b32_e32 v161, 0xffff0000, v54
	v_lshlrev_b32_e32 v162, 16, v55
	v_and_b32_e32 v163, 0xffff0000, v55
	v_lshlrev_b32_e32 v164, 16, v56
	v_and_b32_e32 v165, 0xffff0000, v56
	v_lshlrev_b32_e32 v166, 16, v57
	v_and_b32_e32 v167, 0xffff0000, v57
	v_pk_add_f32 v[176:177], v[176:177], v[160:161]
	v_pk_add_f32 v[178:179], v[178:179], v[162:163]
	v_pk_add_f32 v[180:181], v[180:181], v[164:165]
	v_pk_add_f32 v[182:183], v[182:183], v[166:167]
	v_pk_add_f32 v[176:177], v[176:177], v[128:129] neg_lo:[0,1] neg_hi:[0,1]
	v_pk_add_f32 v[178:179], v[178:179], v[130:131] neg_lo:[0,1] neg_hi:[0,1]
	v_pk_add_f32 v[180:181], v[180:181], v[132:133] neg_lo:[0,1] neg_hi:[0,1]
	v_pk_add_f32 v[182:183], v[182:183], v[134:135] neg_lo:[0,1] neg_hi:[0,1]
	v_pk_fma_f32 v[194:195], v[176:177], v[192:193], v[160:161] neg_lo:[0,0,1] neg_hi:[0,0,1]
	v_pk_fma_f32 v[196:197], v[178:179], v[192:193], v[162:163] neg_lo:[0,0,1] neg_hi:[0,0,1]
	v_pk_fma_f32 v[198:199], v[180:181], v[192:193], v[164:165] neg_lo:[0,0,1] neg_hi:[0,0,1]
	v_pk_fma_f32 v[200:201], v[182:183], v[192:193], v[166:167] neg_lo:[0,0,1] neg_hi:[0,0,1]
	v_cvt_pk_bf16_f32 v184, v194, v195
	v_cvt_pk_bf16_f32 v185, v196, v197
	v_cvt_pk_bf16_f32 v186, v198, v199
	v_cvt_pk_bf16_f32 v187, v200, v201
	global_store_dwordx4 v7, v[184:187], s[14:15]
	s_add_u32 s14, s14, 0x800
	s_addc_u32 s15, s15, 0
	s_waitcnt vmcnt(7)
	v_lshlrev_b32_e32 v168, 16, v58
	v_and_b32_e32 v169, 0xffff0000, v58
	v_lshlrev_b32_e32 v170, 16, v59
	v_and_b32_e32 v171, 0xffff0000, v59
	v_lshlrev_b32_e32 v172, 16, v60
	v_and_b32_e32 v173, 0xffff0000, v60
	v_lshlrev_b32_e32 v174, 16, v61
	v_and_b32_e32 v175, 0xffff0000, v61
	v_pk_add_f32 v[176:177], v[176:177], v[168:169]
	v_pk_add_f32 v[178:179], v[178:179], v[170:171]
	v_pk_add_f32 v[180:181], v[180:181], v[172:173]
	v_pk_add_f32 v[182:183], v[182:183], v[174:175]
	v_pk_add_f32 v[176:177], v[176:177], v[136:137] neg_lo:[0,1] neg_hi:[0,1]
	v_pk_add_f32 v[178:179], v[178:179], v[138:139] neg_lo:[0,1] neg_hi:[0,1]
	v_pk_add_f32 v[180:181], v[180:181], v[140:141] neg_lo:[0,1] neg_hi:[0,1]
	v_pk_add_f32 v[182:183], v[182:183], v[142:143] neg_lo:[0,1] neg_hi:[0,1]
	v_pk_fma_f32 v[194:195], v[176:177], v[192:193], v[168:169] neg_lo:[0,0,1] neg_hi:[0,0,1]
	v_pk_fma_f32 v[196:197], v[178:179], v[192:193], v[170:171] neg_lo:[0,0,1] neg_hi:[0,0,1]
	v_pk_fma_f32 v[198:199], v[180:181], v[192:193], v[172:173] neg_lo:[0,0,1] neg_hi:[0,0,1]
	v_pk_fma_f32 v[200:201], v[182:183], v[192:193], v[174:175] neg_lo:[0,0,1] neg_hi:[0,0,1]
	v_cvt_pk_bf16_f32 v188, v194, v195
	v_cvt_pk_bf16_f32 v189, v196, v197
	v_cvt_pk_bf16_f32 v190, v198, v199
	v_cvt_pk_bf16_f32 v191, v200, v201
	global_store_dwordx4 v7, v[188:191], s[14:15]
	s_add_u32 s14, s14, 0x800
	s_addc_u32 s15, s15, 0
	s_waitcnt vmcnt(7)
; __device__ __forceinline__ unsigned cvt_pk_bf16(float lo, float hi) { unsigned r; asm volatile("v_cvt_pk_bf16_f32 %0, %1, %2" : "=v"(r) : "v"(lo), "v"(hi)); return r; }
; __device__ __forceinline__ void pool_diffs(const bf16_t* Z, bf16_t* DP, int G) {
;     ...
;         for (int k = 0; k < 16; ++k) { s[0] += bf_lo(v[k].x); s[1] += bf_hi(v[k].x); s[2] += bf_lo(v[k].y); s[3] += bf_hi(v[k].y); s[4] += bf_lo(v[k].z); s[5] += bf_hi(v[k].z); s[6] += bf_lo(v[k].w); s[7] += bf_hi(v[k].w); }
;         const float ic = 1.0f / (float)cnt; u32x4 o; const u32x4 c0 = v[0];
;         o.x = cvt_pk_bf16(s[0] * ic - bf_lo(c0.x), s[1] * ic - bf_hi(c0.x)); o.y = cvt_pk_bf16(s[2] * ic - bf_lo(c0.y), s[3] * ic - bf_hi(c0.y));
;         o.z = cvt_pk_bf16(s[4] * ic - bf_lo(c0.z), s[5] * ic - bf_hi(c0.z)); o.w = cvt_pk_bf16(s[6] * ic - bf_lo(c0.w), s[7] * ic - bf_hi(c0.w));
;         *(u32x4*)(DP + (size_t)t * 1024 + col) = o;
	v_lshlrev_b32_e32 v160, 16, v62
	v_and_b32_e32 v161, 0xffff0000, v62
	v_lshlrev_b32_e32 v162, 16, v63
	v_and_b32_e32 v163, 0xffff0000, v63
	v_lshlrev_b32_e32 v164, 16, v64
	v_and_b32_e32 v165, 0xffff0000, v64
	v_lshlrev_b32_e32 v166, 16, v65
	v_and_b32_e32 v167, 0xffff0000, v65
	v_pk_add_f32 v[176:177], v[176:177], v[160:161]
	v_pk_add_f32 v[178:179], v[178:179], v[162:163]
	v_pk_add_f32 v[180:181], v[180:181], v[164:165]
	v_pk_add_f32 v[182:183], v[182:183], v[166:167]
	v_pk_add_f32 v[176:177], v[176:177], v[144:145] neg_lo:[0,1] neg_hi:[0,1]
	v_pk_add_f32 v[178:179], v[178:179], v[146:147] neg_lo:[0,1] neg_hi:[0,1]
	v_pk_add_f32 v[180:181], v[180:181], v[148:149] neg_lo:[0,1] neg_hi:[0,1]
	v_pk_add_f32 v[182:183], v[182:183], v[150:151] neg_lo:[0,1] neg_hi:[0,1]
	v_pk_fma_f32 v[194:195], v[176:177], v[192:193], v[160:161] neg_lo:[0,0,1] neg_hi:[0,0,1]
	v_pk_fma_f32 v[196:197], v[178:179], v[192:193], v[162:163] neg_lo:[0,0,1] neg_hi:[0,0,1]
	v_pk_fma_f32 v[198:199], v[180:181], v[192:193], v[164:165] neg_lo:[0,0,1] neg_hi:[0,0,1]
	v_pk_fma_f32 v[200:201], v[182:183], v[192:193], v[166:167] neg_lo:[0,0,1] neg_hi:[0,0,1]
	v_cvt_pk_bf16_f32 v184, v194, v195
	v_cvt_pk_bf16_f32 v185, v196, v197
	v_cvt_pk_bf16_f32 v186, v198, v199
	v_cvt_pk_bf16_f32 v187, v200, v201
	global_store_dwordx4 v7, v[184:187], s[14:15]
	s_add_u32 s14, s14, 0x800
	s_addc_u32 s15, s15, 0
	s_waitcnt vmcnt(7)
	v_lshlrev_b32_e32 v168, 16, v66
	v_and_b32_e32 v169, 0xffff0000, v66
	v_lshlrev_b32_e32 v170, 16, v67
	v_and_b32_e32 v171, 0xffff0000, v67
	v_lshlrev_b32_e32 v172, 16, v68
	v_and_b32_e32 v173, 0xffff0000, v68
	v_lshlrev_b32_e32 v174, 16, v69
	v_and_b32_e32 v175, 0xffff0000, v69
	v_pk_add_f32 v[176:177], v[176:177], v[168:169]
	v_pk_add_f32 v[178:179], v[178:179], v[170:171]
	v_pk_add_f32 v[180:181], v[180:181], v[172:173]
	v_pk_add_f32 v[182:183], v[182:183], v[174:175]
	v_pk_add_f32 v[176:177], v[176:177], v[152:153] neg_lo:[0,1] neg_hi:[0,1]
	v_pk_add_f32 v[178:179], v[178:179], v[154:155] neg_lo:[0,1] neg_hi:[0,1]
	v_pk_add_f32 v[180:181], v[180:181], v[156:157] neg_lo:[0,1] neg_hi:[0,1]
	v_pk_add_f32 v[182:183], v[182:183], v[158:159] neg_lo:[0,1] neg_hi:[0,1]
	v_pk_fma_f32 v[194:195], v[176:177], v[192:193], v[168:169] neg_lo:[0,0,1] neg_hi:[0,0,1]
	v_pk_fma_f32 v[196:197], v[178:179], v[192:193], v[170:171] neg_lo:[0,0,1] neg_hi:[0,0,1]
	v_pk_fma_f32 v[198:199], v[180:181], v[192:193], v[172:173] neg_lo:[0,0,1] neg_hi:[0,0,1]
	v_pk_fma_f32 v[200:201], v[182:183], v[192:193], v[174:175] neg_lo:[0,0,1] neg_hi:[0,0,1]
	v_cvt_pk_bf16_f32 v188, v194, v195
	v_cvt_pk_bf16_f32 v189, v196, v197
	v_cvt_pk_bf16_f32 v190, v198, v199
	v_cvt_pk_bf16_f32 v191, v200, v201
	global_store_dwordx4 v7, v[188:191], s[14:15]
	s_branch .Lpd2_next
.Lpd2_w4:
	v_mov_b32_e32 v192, 0x3e800000
	v_mov_b32_e32 v193, 0x3e800000
	global_load_dwordx4 v[10:13], v6, s[12:13]
	s_add_u32 s12, s12, 0x2800
	s_addc_u32 s13, s13, 0
	global_load_dwordx4 v[14:17], v6, s[12:13]
	s_add_u32 s12, s12, 0x2800
	s_addc_u32 s13, s13, 0
	global_load_dwordx4 v[18:21], v6, s[12:13]
	s_add_u32 s12, s12, 0x2800
	s_addc_u32 s13, s13, 0
	global_load_dwordx4 v[22:25], v6, s[12:13]
	s_add_u32 s12, s12, 0x2800
	s_addc_u32 s13, s13, 0
	global_load_dwordx4 v[26:29], v6, s[12:13]
	s_add_u32 s12, s12, 0x2800
	s_addc_u32 s13, s13, 0
	global_load_dwordx4 v[30:33], v6, s[12:13]
	s_add_u32 s12, s12, 0x2800
	s_addc_u32 s13, s13, 0
	global_load_dwordx4 v[34:37], v6, s[12:13]
	s_add_u32 s12, s12, 0x2800
	s_addc_u32 s13, s13, 0
	global_load_dwordx4 v[38:41], v6, s[12:13]
	s_add_u32 s12, s12, 0x2800
	s_addc_u32 s13, s13, 0
	global_load_dwordx4 v[42:45], v6, s[12:13]
	s_add_u32 s12, s12, 0x2800
	s_addc_u32 s13, s13, 0
	global_load_dwordx4 v[46:49], v6, s[12:13]
	s_add_u32 s12, s12, 0x2800
	s_addc_u32 s13, s13, 0
	global_load_dwordx4 v[50:53], v6, s[12:13]
	s_waitcnt vmcnt(10)
	v_lshlrev_b32_e32 v104, 16, v10
	v_and_b32_e32 v105, 0xffff0000, v10
	v_lshlrev_b32_e32 v106, 16, v11
	v_and_b32_e32 v107, 0xffff0000, v11
	v_lshlrev_b32_e32 v108, 16, v12
	v_and_b32_e32 v109, 0xffff0000, v12
	v_lshlrev_b32_e32 v110, 16, v13
	v_and_b32_e32 v111, 0xffff0000, v13
	s_waitcnt vmcnt(9)
	v_lshlrev_b32_e32 v112, 16, v14
	v_and_b32_e32 v113, 0xffff0000, v14
	v_lshlrev_b32_e32 v114, 16, v15
	v_and_b32_e32 v115, 0xffff0000, v15
	v_lshlrev_b32_e32 v116, 16, v16
	v_and_b32_e32 v117, 0xffff0000, v16
	v_lshlrev_b32_e32 v118, 16, v17
	v_and_b32_e32 v119, 0xffff0000, v17
	v_pk_add_f32 v[176:177], v[104:105], v[112:113]
	v_pk_add_f32 v[178:179], v[106:107], v[114:115]
	v_pk_add_f32 v[180:181], v[108:109], v[116:117]
	v_pk_add_f32 v[182:183], v[110:111], v[118:119]
	s_waitcnt vmcnt(8)
	v_lshlrev_b32_e32 v120, 16, v18
	v_and_b32_e32 v121, 0xffff0000, v18
	v_lshlrev_b32_e32 v122, 16, v19
	v_and_b32_e32 v123, 0xffff0000, v19
	v_lshlrev_b32_e32 v124, 16, v20
	v_and_b32_e32 v125, 0xffff0000, v20
	v_lshlrev_b32_e32 v126, 16, v21
	v_and_b32_e32 v127, 0xffff0000, v21
	v_pk_add_f32 v[176:177], v[176:177], v[120:121]
	v_pk_add_f32 v[178:179], v[178:179], v[122:123]
	v_pk_add_f32 v[180:181], v[180:181], v[124:125]
	v_pk_add_f32 v[182:183], v[182:183], v[126:127]
	s_waitcnt vmcnt(7)
; __device__ __forceinline__ unsigned cvt_pk_bf16(float lo, float hi) { unsigned r; asm volatile("v_cvt_pk_bf16_f32 %0, %1, %2" : "=v"(r) : "v"(lo), "v"(hi)); return r; }
; __device__ __forceinline__ void pool_diffs(const bf16_t* Z, bf16_t* DP, int G) {
;     ...
;         for (int k = 0; k < 16; ++k) { s[0] += bf_lo(v[k].x); s[1] += bf_hi(v[k].x); s[2] += bf_lo(v[k].y); s[3] += bf_hi(v[k].y); s[4] += bf_lo(v[k].z); s[5] += bf_hi(v[k].z); s[6] += bf_lo(v[k].w); s[7] += bf_hi(v[k].w); }
;         const float ic = 1.0f / (float)cnt; u32x4 o; const u32x4 c0 = v[0];
;         o.x = cvt_pk_bf16(s[0] * ic - bf_lo(c0.x), s[1] * ic - bf_hi(c0.x)); o.y = cvt_pk_bf16(s[2] * ic - bf_lo(c0.y), s[3] * ic - bf_hi(c0.y));
;         o.z = cvt_pk_bf16(s[4] * ic - bf_lo(c0.z), s[5] * ic - bf_hi(c0.z)); o.w = cvt_pk_bf16(s[6] * ic - bf_lo(c0.w), s[7] * ic - bf_hi(c0.w));
;         *(u32x4*)(DP + (size_t)t * 1024 + col) = o;
	v_lshlrev_b32_e32 v128, 16, v22
	v_and_b32_e32 v129, 0xffff0000, v22
	v_lshlrev_b32_e32 v130, 16, v23
	v_and_b32_e32 v131, 0xffff0000, v23
	v_lshlrev_b32_e32 v132, 16, v24
	v_and_b32_e32 v133, 0xffff0000, v24
	v_lshlrev_b32_e32 v134, 16, v25
	v_and_b32_e32 v135, 0xffff0000, v25
	v_pk_add_f32 v[176:177], v[176:177], v[128:129]
	v_pk_add_f32 v[178:179], v[178:179], v[130:131]
	v_pk_add_f32 v[180:181], v[180:181], v[132:133]
	v_pk_add_f32 v[182:183], v[182:183], v[134:135]
	v_pk_fma_f32 v[194:195], v[176:177], v[192:193], v[128:129] neg_lo:[0,0,1] neg_hi:[0,0,1]
	v_pk_fma_f32 v[196:197], v[178:179], v[192:193], v[130:131] neg_lo:[0,0,1] neg_hi:[0,0,1]
	v_pk_fma_f32 v[198:199], v[180:181], v[192:193], v[132:133] neg_lo:[0,0,1] neg_hi:[0,0,1]
	v_pk_fma_f32 v[200:201], v[182:183], v[192:193], v[134:135] neg_lo:[0,0,1] neg_hi:[0,0,1]
	v_cvt_pk_bf16_f32 v184, v194, v195
	v_cvt_pk_bf16_f32 v185, v196, v197
	v_cvt_pk_bf16_f32 v186, v198, v199
	v_cvt_pk_bf16_f32 v187, v200, v201
	global_store_dwordx4 v7, v[184:187], s[14:15]
	s_add_u32 s14, s14, 0x800
	s_addc_u32 s15, s15, 0
	s_waitcnt vmcnt(7)
	v_lshlrev_b32_e32 v136, 16, v26
	v_and_b32_e32 v137, 0xffff0000, v26
	v_lshlrev_b32_e32 v138, 16, v27
	v_and_b32_e32 v139, 0xffff0000, v27
	v_lshlrev_b32_e32 v140, 16, v28
	v_and_b32_e32 v141, 0xffff0000, v28
	v_lshlrev_b32_e32 v142, 16, v29
	v_and_b32_e32 v143, 0xffff0000, v29
	v_pk_add_f32 v[176:177], v[176:177], v[136:137]
	v_pk_add_f32 v[178:179], v[178:179], v[138:139]
	v_pk_add_f32 v[180:181], v[180:181], v[140:141]
	v_pk_add_f32 v[182:183], v[182:183], v[142:143]
	v_pk_add_f32 v[176:177], v[176:177], v[104:105] neg_lo:[0,1] neg_hi:[0,1]
	v_pk_add_f32 v[178:179], v[178:179], v[106:107] neg_lo:[0,1] neg_hi:[0,1]
	v_pk_add_f32 v[180:181], v[180:181], v[108:109] neg_lo:[0,1] neg_hi:[0,1]
	v_pk_add_f32 v[182:183], v[182:183], v[110:111] neg_lo:[0,1] neg_hi:[0,1]
	v_pk_fma_f32 v[194:195], v[176:177], v[192:193], v[136:137] neg_lo:[0,0,1] neg_hi:[0,0,1]
	v_pk_fma_f32 v[196:197], v[178:179], v[192:193], v[138:139] neg_lo:[0,0,1] neg_hi:[0,0,1]
	v_pk_fma_f32 v[198:199], v[180:181], v[192:193], v[140:141] neg_lo:[0,0,1] neg_hi:[0,0,1]
	v_pk_fma_f32 v[200:201], v[182:183], v[192:193], v[142:143] neg_lo:[0,0,1] neg_hi:[0,0,1]
	v_cvt_pk_bf16_f32 v188, v194, v195
	v_cvt_pk_bf16_f32 v189, v196, v197
	v_cvt_pk_bf16_f32 v190, v198, v199
	v_cvt_pk_bf16_f32 v191, v200, v201
	global_store_dwordx4 v7, v[188:191], s[14:15]
	s_add_u32 s14, s14, 0x800
	s_addc_u32 s15, s15, 0
	s_waitcnt vmcnt(7)
	v_lshlrev_b32_e32 v144, 16, v30
	v_and_b32_e32 v145, 0xffff0000, v30
	v_lshlrev_b32_e32 v146, 16, v31
	v_and_b32_e32 v147, 0xffff0000, v31
	v_lshlrev_b32_e32 v148, 16, v32
	v_and_b32_e32 v149, 0xffff0000, v32
	v_lshlrev_b32_e32 v150, 16, v33
	v_and_b32_e32 v151, 0xffff0000, v33
	v_pk_add_f32 v[176:177], v[176:177], v[144:145]
	v_pk_add_f32 v[178:179], v[178:179], v[146:147]
	v_pk_add_f32 v[180:181], v[180:181], v[148:149]
	v_pk_add_f32 v[182:183], v[182:183], v[150:151]
	v_pk_add_f32 v[176:177], v[176:177], v[112:113] neg_lo:[0,1] neg_hi:[0,1]
	v_pk_add_f32 v[178:179], v[178:179], v[114:115] neg_lo:[0,1] neg_hi:[0,1]
	v_pk_add_f32 v[180:181], v[180:181], v[116:117] neg_lo:[0,1] neg_hi:[0,1]
	v_pk_add_f32 v[182:183], v[182:183], v[118:119] neg_lo:[0,1] neg_hi:[0,1]
	v_pk_fma_f32 v[194:195], v[176:177], v[192:193], v[144:145] neg_lo:[0,0,1] neg_hi:[0,0,1]
	v_pk_fma_f32 v[196:197], v[178:179], v[192:193], v[146:147] neg_lo:[0,0,1] neg_hi:[0,0,1]
	v_pk_fma_f32 v[198:199], v[180:181], v[192:193], v[148:149] neg_lo:[0,0,1] neg_hi:[0,0,1]
	v_pk_fma_f32 v[200:201], v[182:183], v[192:193], v[150:151] neg_lo:[0,0,1] neg_hi:[0,0,1]
	v_cvt_pk_bf16_f32 v184, v194, v195
	v_cvt_pk_bf16_f32 v185, v196, v197
	v_cvt_pk_bf16_f32 v186, v198, v199
	v_cvt_pk_bf16_f32 v187, v200, v201
	global_store_dwordx4 v7, v[184:187], s[14:15]
	s_add_u32 s14, s14, 0x800
	s_addc_u32 s15, s15, 0
	s_waitcnt vmcnt(7)
	v_lshlrev_b32_e32 v152, 16, v34
	v_and_b32_e32 v153, 0xffff0000, v34
	v_lshlrev_b32_e32 v154, 16, v35
	v_and_b32_e32 v155, 0xffff0000, v35
	v_lshlrev_b32_e32 v156, 16, v36
	v_and_b32_e32 v157, 0xffff0000, v36
	v_lshlrev_b32_e32 v158, 16, v37
	v_and_b32_e32 v159, 0xffff0000, v37
	v_pk_add_f32 v[176:177], v[176:177], v[152:153]
	v_pk_add_f32 v[178:179], v[178:179], v[154:155]
	v_pk_add_f32 v[180:181], v[180:181], v[156:157]
	v_pk_add_f32 v[182:183], v[182:183], v[158:159]
	v_pk_add_f32 v[176:177], v[176:177], v[120:121] neg_lo:[0,1] neg_hi:[0,1]
	v_pk_add_f32 v[178:179], v[178:179], v[122:123] neg_lo:[0,1] neg_hi:[0,1]
	v_pk_add_f32 v[180:181], v[180:181], v[124:125] neg_lo:[0,1] neg_hi:[0,1]
	v_pk_add_f32 v[182:183], v[182:183], v[126:127] neg_lo:[0,1] neg_hi:[0,1]
	v_pk_fma_f32 v[194:195], v[176:177], v[192:193], v[152:153] neg_lo:[0,0,1] neg_hi:[0,0,1]
	v_pk_fma_f32 v[196:197], v[178:179], v[192:193], v[154:155] neg_lo:[0,0,1] neg_hi:[0,0,1]
	v_pk_fma_f32 v[198:199], v[180:181], v[192:193], v[156:157] neg_lo:[0,0,1] neg_hi:[0,0,1]
	v_pk_fma_f32 v[200:201], v[182:183], v[192:193], v[158:159] neg_lo:[0,0,1] neg_hi:[0,0,1]
	v_cvt_pk_bf16_f32 v188, v194, v195
	v_cvt_pk_bf16_f32 v189, v196, v197
	v_cvt_pk_bf16_f32 v190, v198, v199
	v_cvt_pk_bf16_f32 v191, v200, v201
	global_store_dwordx4 v7, v[188:191], s[14:15]
	s_add_u32 s14, s14, 0x800
	s_addc_u32 s15, s15, 0
	s_waitcnt vmcnt(7)
; __device__ __forceinline__ unsigned cvt_pk_bf16(float lo, float hi) { unsigned r; asm volatile("v_cvt_pk_bf16_f32 %0, %1, %2" : "=v"(r) : "v"(lo), "v"(hi)); return r; }
; __device__ __forceinline__ void pool_diffs(const bf16_t* Z, bf16_t* DP, int G) {
;     ...
;         for (int k = 0; k < 16; ++k) { s[0] += bf_lo(v[k].x); s[1] += bf_hi(v[k].x); s[2] += bf_lo(v[k].y); s[3] += bf_hi(v[k].y); s[4] += bf_lo(v[k].z); s[5] += bf_hi(v[k].z); s[6] += bf_lo(v[k].w); s[7] += bf_hi(v[k].w); }
;         const float ic = 1.0f / (float)cnt; u32x4 o; const u32x4 c0 = v[0];
;         o.x = cvt_pk_bf16(s[0] * ic - bf_lo(c0.x), s[1] * ic - bf_hi(c0.x)); o.y = cvt_pk_bf16(s[2] * ic - bf_lo(c0.y), s[3] * ic - bf_hi(c0.y));
;         o.z = cvt_pk_bf16(s[4] * ic - bf_lo(c0.z), s[5] * ic - bf_hi(c0.z)); o.w = cvt_pk_bf16(s[6] * ic - bf_lo(c0.w), s[7] * ic - bf_hi(c0.w));
;         *(u32x4*)(DP + (size_t)t * 1024 + col) = o;
	v_lshlrev_b32_e32 v160, 16, v38
	v_and_b32_e32 v161, 0xffff0000, v38
	v_lshlrev_b32_e32 v162, 16, v39
	v_and_b32_e32 v163, 0xffff0000, v39
	v_lshlrev_b32_e32 v164, 16, v40
	v_and_b32_e32 v165, 0xffff0000, v40
	v_lshlrev_b32_e32 v166, 16, v41
	v_and_b32_e32 v167, 0xffff0000, v41
	v_pk_add_f32 v[176:177], v[176:177], v[160:161]
	v_pk_add_f32 v[178:179], v[178:179], v[162:163]
	v_pk_add_f32 v[180:181], v[180:181], v[164:165]
	v_pk_add_f32 v[182:183], v[182:183], v[166:167]
	v_pk_add_f32 v[176:177], v[176:177], v[128:129] neg_lo:[0,1] neg_hi:[0,1]
	v_pk_add_f32 v[178:179], v[178:179], v[130:131] neg_lo:[0,1] neg_hi:[0,1]
	v_pk_add_f32 v[180:181], v[180:181], v[132:133] neg_lo:[0,1] neg_hi:[0,1]
	v_pk_add_f32 v[182:183], v[182:183], v[134:135] neg_lo:[0,1] neg_hi:[0,1]
	v_pk_fma_f32 v[194:195], v[176:177], v[192:193], v[160:161] neg_lo:[0,0,1] neg_hi:[0,0,1]
	v_pk_fma_f32 v[196:197], v[178:179], v[192:193], v[162:163] neg_lo:[0,0,1] neg_hi:[0,0,1]
	v_pk_fma_f32 v[198:199], v[180:181], v[192:193], v[164:165] neg_lo:[0,0,1] neg_hi:[0,0,1]
	v_pk_fma_f32 v[200:201], v[182:183], v[192:193], v[166:167] neg_lo:[0,0,1] neg_hi:[0,0,1]
	v_cvt_pk_bf16_f32 v184, v194, v195
	v_cvt_pk_bf16_f32 v185, v196, v197
	v_cvt_pk_bf16_f32 v186, v198, v199
	v_cvt_pk_bf16_f32 v187, v200, v201
	global_store_dwordx4 v7, v[184:187], s[14:15]
	s_add_u32 s14, s14, 0x800
	s_addc_u32 s15, s15, 0
	s_waitcnt vmcnt(7)
	v_lshlrev_b32_e32 v168, 16, v42
	v_and_b32_e32 v169, 0xffff0000, v42
	v_lshlrev_b32_e32 v170, 16, v43
	v_and_b32_e32 v171, 0xffff0000, v43
	v_lshlrev_b32_e32 v172, 16, v44
	v_and_b32_e32 v173, 0xffff0000, v44
	v_lshlrev_b32_e32 v174, 16, v45
	v_and_b32_e32 v175, 0xffff0000, v45
	v_pk_add_f32 v[176:177], v[176:177], v[168:169]
	v_pk_add_f32 v[178:179], v[178:179], v[170:171]
	v_pk_add_f32 v[180:181], v[180:181], v[172:173]
	v_pk_add_f32 v[182:183], v[182:183], v[174:175]
	v_pk_add_f32 v[176:177], v[176:177], v[136:137] neg_lo:[0,1] neg_hi:[0,1]
	v_pk_add_f32 v[178:179], v[178:179], v[138:139] neg_lo:[0,1] neg_hi:[0,1]
	v_pk_add_f32 v[180:181], v[180:181], v[140:141] neg_lo:[0,1] neg_hi:[0,1]
	v_pk_add_f32 v[182:183], v[182:183], v[142:143] neg_lo:[0,1] neg_hi:[0,1]
	v_pk_fma_f32 v[194:195], v[176:177], v[192:193], v[168:169] neg_lo:[0,0,1] neg_hi:[0,0,1]
	v_pk_fma_f32 v[196:197], v[178:179], v[192:193], v[170:171] neg_lo:[0,0,1] neg_hi:[0,0,1]
	v_pk_fma_f32 v[198:199], v[180:181], v[192:193], v[172:173] neg_lo:[0,0,1] neg_hi:[0,0,1]
	v_pk_fma_f32 v[200:201], v[182:183], v[192:193], v[174:175] neg_lo:[0,0,1] neg_hi:[0,0,1]
	v_cvt_pk_bf16_f32 v188, v194, v195
	v_cvt_pk_bf16_f32 v189, v196, v197
	v_cvt_pk_bf16_f32 v190, v198, v199
	v_cvt_pk_bf16_f32 v191, v200, v201
	global_store_dwordx4 v7, v[188:191], s[14:15]
	s_add_u32 s14, s14, 0x800
	s_addc_u32 s15, s15, 0
	s_waitcnt vmcnt(7)
	v_lshlrev_b32_e32 v160, 16, v46
	v_and_b32_e32 v161, 0xffff0000, v46
	v_lshlrev_b32_e32 v162, 16, v47
	v_and_b32_e32 v163, 0xffff0000, v47
	v_lshlrev_b32_e32 v164, 16, v48
	v_and_b32_e32 v165, 0xffff0000, v48
	v_lshlrev_b32_e32 v166, 16, v49
	v_and_b32_e32 v167, 0xffff0000, v49
	v_pk_add_f32 v[176:177], v[176:177], v[160:161]
	v_pk_add_f32 v[178:179], v[178:179], v[162:163]
	v_pk_add_f32 v[180:181], v[180:181], v[164:165]
	v_pk_add_f32 v[182:183], v[182:183], v[166:167]
	v_pk_add_f32 v[176:177], v[176:177], v[144:145] neg_lo:[0,1] neg_hi:[0,1]
	v_pk_add_f32 v[178:179], v[178:179], v[146:147] neg_lo:[0,1] neg_hi:[0,1]
	v_pk_add_f32 v[180:181], v[180:181], v[148:149] neg_lo:[0,1] neg_hi:[0,1]
	v_pk_add_f32 v[182:183], v[182:183], v[150:151] neg_lo:[0,1] neg_hi:[0,1]
	v_pk_fma_f32 v[194:195], v[176:177], v[192:193], v[160:161] neg_lo:[0,0,1] neg_hi:[0,0,1]
	v_pk_fma_f32 v[196:197], v[178:179], v[192:193], v[162:163] neg_lo:[0,0,1] neg_hi:[0,0,1]
	v_pk_fma_f32 v[198:199], v[180:181], v[192:193], v[164:165] neg_lo:[0,0,1] neg_hi:[0,0,1]
	v_pk_fma_f32 v[200:201], v[182:183], v[192:193], v[166:167] neg_lo:[0,0,1] neg_hi:[0,0,1]
	v_cvt_pk_bf16_f32 v184, v194, v195
	v_cvt_pk_bf16_f32 v185, v196, v197
	v_cvt_pk_bf16_f32 v186, v198, v199
	v_cvt_pk_bf16_f32 v187, v200, v201
	global_store_dwordx4 v7, v[184:187], s[14:15]
	s_add_u32 s14, s14, 0x800
	s_addc_u32 s15, s15, 0
	s_waitcnt vmcnt(7)
	v_lshlrev_b32_e32 v168, 16, v50
	v_and_b32_e32 v169, 0xffff0000, v50
	v_lshlrev_b32_e32 v170, 16, v51
	v_and_b32_e32 v171, 0xffff0000, v51
	v_lshlrev_b32_e32 v172, 16, v52
	v_and_b32_e32 v173, 0xffff0000, v52
	v_lshlrev_b32_e32 v174, 16, v53
	v_and_b32_e32 v175, 0xffff0000, v53
	v_pk_add_f32 v[176:177], v[176:177], v[168:169]
	v_pk_add_f32 v[178:179], v[178:179], v[170:171]
	v_pk_add_f32 v[180:181], v[180:181], v[172:173]
	v_pk_add_f32 v[182:183], v[182:183], v[174:175]
	v_pk_add_f32 v[176:177], v[176:177], v[152:153] neg_lo:[0,1] neg_hi:[0,1]
	v_pk_add_f32 v[178:179], v[178:179], v[154:155] neg_lo:[0,1] neg_hi:[0,1]
	v_pk_add_f32 v[180:181], v[180:181], v[156:157] neg_lo:[0,1] neg_hi:[0,1]
	v_pk_add_f32 v[182:183], v[182:183], v[158:159] neg_lo:[0,1] neg_hi:[0,1]
	v_pk_fma_f32 v[194:195], v[176:177], v[192:193], v[168:169] neg_lo:[0,0,1] neg_hi:[0,0,1]
	v_pk_fma_f32 v[196:197], v[178:179], v[192:193], v[170:171] neg_lo:[0,0,1] neg_hi:[0,0,1]
	v_pk_fma_f32 v[198:199], v[180:181], v[192:193], v[172:173] neg_lo:[0,0,1] neg_hi:[0,0,1]
	v_pk_fma_f32 v[200:201], v[182:183], v[192:193], v[174:175] neg_lo:[0,0,1] neg_hi:[0,0,1]
	v_cvt_pk_bf16_f32 v188, v194, v195
	v_cvt_pk_bf16_f32 v189, v196, v197
	v_cvt_pk_bf16_f32 v190, v198, v199
	v_cvt_pk_bf16_f32 v191, v200, v201
	global_store_dwordx4 v7, v[188:191], s[14:15]
	s_branch .Lpd2_next
; __device__ __forceinline__ unsigned cvt_pk_bf16(float lo, float hi) { unsigned r; asm volatile("v_cvt_pk_bf16_f32 %0, %1, %2" : "=v"(r) : "v"(lo), "v"(hi)); return r; }
; __device__ __forceinline__ void pool_diffs(const bf16_t* Z, bf16_t* DP, int G) {
;     ...
;         for (int k = 0; k < 16; ++k) { s[0] += bf_lo(v[k].x); s[1] += bf_hi(v[k].x); s[2] += bf_lo(v[k].y); s[3] += bf_hi(v[k].y); s[4] += bf_lo(v[k].z); s[5] += bf_hi(v[k].z); s[6] += bf_lo(v[k].w); s[7] += bf_hi(v[k].w); }
;         const float ic = 1.0f / (float)cnt; u32x4 o; const u32x4 c0 = v[0];
;         o.x = cvt_pk_bf16(s[0] * ic - bf_lo(c0.x), s[1] * ic - bf_hi(c0.x)); o.y = cvt_pk_bf16(s[2] * ic - bf_lo(c0.y), s[3] * ic - bf_hi(c0.y));
;         o.z = cvt_pk_bf16(s[4] * ic - bf_lo(c0.z), s[5] * ic - bf_hi(c0.z)); o.w = cvt_pk_bf16(s[6] * ic - bf_lo(c0.w), s[7] * ic - bf_hi(c0.w));
;         *(u32x4*)(DP + (size_t)t * 1024 + col) = o;
.Lpd2_w2:
	v_mov_b32_e32 v192, 0.5
	v_mov_b32_e32 v193, 0.5
	global_load_dwordx4 v[10:13], v6, s[12:13]
	s_add_u32 s12, s12, 0x2800
	s_addc_u32 s13, s13, 0
	global_load_dwordx4 v[14:17], v6, s[12:13]
	s_add_u32 s12, s12, 0x2800
	s_addc_u32 s13, s13, 0
	global_load_dwordx4 v[18:21], v6, s[12:13]
	s_add_u32 s12, s12, 0x2800
	s_addc_u32 s13, s13, 0
	global_load_dwordx4 v[22:25], v6, s[12:13]
	s_add_u32 s12, s12, 0x2800
	s_addc_u32 s13, s13, 0
	global_load_dwordx4 v[26:29], v6, s[12:13]
	s_add_u32 s12, s12, 0x2800
	s_addc_u32 s13, s13, 0
	global_load_dwordx4 v[30:33], v6, s[12:13]
	s_add_u32 s12, s12, 0x2800
	s_addc_u32 s13, s13, 0
	global_load_dwordx4 v[34:37], v6, s[12:13]
	s_add_u32 s12, s12, 0x2800
	s_addc_u32 s13, s13, 0
	global_load_dwordx4 v[38:41], v6, s[12:13]
	s_add_u32 s12, s12, 0x2800
	s_addc_u32 s13, s13, 0
	global_load_dwordx4 v[42:45], v6, s[12:13]
	s_waitcnt vmcnt(8)
	v_lshlrev_b32_e32 v104, 16, v10
	v_and_b32_e32 v105, 0xffff0000, v10
	v_lshlrev_b32_e32 v106, 16, v11
	v_and_b32_e32 v107, 0xffff0000, v11
	v_lshlrev_b32_e32 v108, 16, v12
	v_and_b32_e32 v109, 0xffff0000, v12
	v_lshlrev_b32_e32 v110, 16, v13
	v_and_b32_e32 v111, 0xffff0000, v13
	s_waitcnt vmcnt(7)
	v_lshlrev_b32_e32 v112, 16, v14
	v_and_b32_e32 v113, 0xffff0000, v14
	v_lshlrev_b32_e32 v114, 16, v15
	v_and_b32_e32 v115, 0xffff0000, v15
	v_lshlrev_b32_e32 v116, 16, v16
	v_and_b32_e32 v117, 0xffff0000, v16
	v_lshlrev_b32_e32 v118, 16, v17
	v_and_b32_e32 v119, 0xffff0000, v17
	v_pk_add_f32 v[176:177], v[104:105], v[112:113]
	v_pk_add_f32 v[178:179], v[106:107], v[114:115]
	v_pk_add_f32 v[180:181], v[108:109], v[116:117]
	v_pk_add_f32 v[182:183], v[110:111], v[118:119]
	v_pk_fma_f32 v[194:195], v[176:177], v[192:193], v[112:113] neg_lo:[0,0,1] neg_hi:[0,0,1]
	v_pk_fma_f32 v[196:197], v[178:179], v[192:193], v[114:115] neg_lo:[0,0,1] neg_hi:[0,0,1]
	v_pk_fma_f32 v[198:199], v[180:181], v[192:193], v[116:117] neg_lo:[0,0,1] neg_hi:[0,0,1]
	v_pk_fma_f32 v[200:201], v[182:183], v[192:193], v[118:119] neg_lo:[0,0,1] neg_hi:[0,0,1]
	v_cvt_pk_bf16_f32 v184, v194, v195
	v_cvt_pk_bf16_f32 v185, v196, v197
	v_cvt_pk_bf16_f32 v186, v198, v199
	v_cvt_pk_bf16_f32 v187, v200, v201
	global_store_dwordx4 v7, v[184:187], s[14:15]
	s_add_u32 s14, s14, 0x800
	s_addc_u32 s15, s15, 0
	s_waitcnt vmcnt(7)
	v_lshlrev_b32_e32 v120, 16, v18
	v_and_b32_e32 v121, 0xffff0000, v18
	v_lshlrev_b32_e32 v122, 16, v19
	v_and_b32_e32 v123, 0xffff0000, v19
	v_lshlrev_b32_e32 v124, 16, v20
	v_and_b32_e32 v125, 0xffff0000, v20
	v_lshlrev_b32_e32 v126, 16, v21
	v_and_b32_e32 v127, 0xffff0000, v21
	v_pk_add_f32 v[176:177], v[176:177], v[120:121]
	v_pk_add_f32 v[178:179], v[178:179], v[122:123]
	v_pk_add_f32 v[180:181], v[180:181], v[124:125]
	v_pk_add_f32 v[182:183], v[182:183], v[126:127]
	v_pk_add_f32 v[176:177], v[176:177], v[104:105] neg_lo:[0,1] neg_hi:[0,1]
	v_pk_add_f32 v[178:179], v[178:179], v[106:107] neg_lo:[0,1] neg_hi:[0,1]
	v_pk_add_f32 v[180:181], v[180:181], v[108:109] neg_lo:[0,1] neg_hi:[0,1]
	v_pk_add_f32 v[182:183], v[182:183], v[110:111] neg_lo:[0,1] neg_hi:[0,1]
	v_pk_fma_f32 v[194:195], v[176:177], v[192:193], v[120:121] neg_lo:[0,0,1] neg_hi:[0,0,1]
	v_pk_fma_f32 v[196:197], v[178:179], v[192:193], v[122:123] neg_lo:[0,0,1] neg_hi:[0,0,1]
	v_pk_fma_f32 v[198:199], v[180:181], v[192:193], v[124:125] neg_lo:[0,0,1] neg_hi:[0,0,1]
	v_pk_fma_f32 v[200:201], v[182:183], v[192:193], v[126:127] neg_lo:[0,0,1] neg_hi:[0,0,1]
	v_cvt_pk_bf16_f32 v188, v194, v195
	v_cvt_pk_bf16_f32 v189, v196, v197
	v_cvt_pk_bf16_f32 v190, v198, v199
	v_cvt_pk_bf16_f32 v191, v200, v201
	global_store_dwordx4 v7, v[188:191], s[14:15]
	s_add_u32 s14, s14, 0x800
	s_addc_u32 s15, s15, 0
	s_waitcnt vmcnt(7)
	v_lshlrev_b32_e32 v128, 16, v22
	v_and_b32_e32 v129, 0xffff0000, v22
	v_lshlrev_b32_e32 v130, 16, v23
	v_and_b32_e32 v131, 0xffff0000, v23
	v_lshlrev_b32_e32 v132, 16, v24
	v_and_b32_e32 v133, 0xffff0000, v24
	v_lshlrev_b32_e32 v134, 16, v25
	v_and_b32_e32 v135, 0xffff0000, v25
	v_pk_add_f32 v[176:177], v[176:177], v[128:129]
	v_pk_add_f32 v[178:179], v[178:179], v[130:131]
	v_pk_add_f32 v[180:181], v[180:181], v[132:133]
	v_pk_add_f32 v[182:183], v[182:183], v[134:135]
	v_pk_add_f32 v[176:177], v[176:177], v[112:113] neg_lo:[0,1] neg_hi:[0,1]
	v_pk_add_f32 v[178:179], v[178:179], v[114:115] neg_lo:[0,1] neg_hi:[0,1]
	v_pk_add_f32 v[180:181], v[180:181], v[116:117] neg_lo:[0,1] neg_hi:[0,1]
	v_pk_add_f32 v[182:183], v[182:183], v[118:119] neg_lo:[0,1] neg_hi:[0,1]
	v_pk_fma_f32 v[194:195], v[176:177], v[192:193], v[128:129] neg_lo:[0,0,1] neg_hi:[0,0,1]
	v_pk_fma_f32 v[196:197], v[178:179], v[192:193], v[130:131] neg_lo:[0,0,1] neg_hi:[0,0,1]
	v_pk_fma_f32 v[198:199], v[180:181], v[192:193], v[132:133] neg_lo:[0,0,1] neg_hi:[0,0,1]
	v_pk_fma_f32 v[200:201], v[182:183], v[192:193], v[134:135] neg_lo:[0,0,1] neg_hi:[0,0,1]
	v_cvt_pk_bf16_f32 v184, v194, v195
	v_cvt_pk_bf16_f32 v185, v196, v197
	v_cvt_pk_bf16_f32 v186, v198, v199
	v_cvt_pk_bf16_f32 v187, v200, v201
	global_store_dwordx4 v7, v[184:187], s[14:15]
	s_add_u32 s14, s14, 0x800
	s_addc_u32 s15, s15, 0
	s_waitcnt vmcnt(7)
; __device__ __forceinline__ unsigned cvt_pk_bf16(float lo, float hi) { unsigned r; asm volatile("v_cvt_pk_bf16_f32 %0, %1, %2" : "=v"(r) : "v"(lo), "v"(hi)); return r; }
; __device__ __forceinline__ void pool_diffs(const bf16_t* Z, bf16_t* DP, int G) {
;     ...
;         for (int k = 0; k < 16; ++k) { s[0] += bf_lo(v[k].x); s[1] += bf_hi(v[k].x); s[2] += bf_lo(v[k].y); s[3] += bf_hi(v[k].y); s[4] += bf_lo(v[k].z); s[5] += bf_hi(v[k].z); s[6] += bf_lo(v[k].w); s[7] += bf_hi(v[k].w); }
;         const float ic = 1.0f / (float)cnt; u32x4 o; const u32x4 c0 = v[0];
;         o.x = cvt_pk_bf16(s[0] * ic - bf_lo(c0.x), s[1] * ic - bf_hi(c0.x)); o.y = cvt_pk_bf16(s[2] * ic - bf_lo(c0.y), s[3] * ic - bf_hi(c0.y));
;         o.z = cvt_pk_bf16(s[4] * ic - bf_lo(c0.z), s[5] * ic - bf_hi(c0.z)); o.w = cvt_pk_bf16(s[6] * ic - bf_lo(c0.w), s[7] * ic - bf_hi(c0.w));
;         *(u32x4*)(DP + (size_t)t * 1024 + col) = o;
	v_lshlrev_b32_e32 v136, 16, v26
	v_and_b32_e32 v137, 0xffff0000, v26
	v_lshlrev_b32_e32 v138, 16, v27
	v_and_b32_e32 v139, 0xffff0000, v27
	v_lshlrev_b32_e32 v140, 16, v28
	v_and_b32_e32 v141, 0xffff0000, v28
	v_lshlrev_b32_e32 v142, 16, v29
	v_and_b32_e32 v143, 0xffff0000, v29
	v_pk_add_f32 v[176:177], v[176:177], v[136:137]
	v_pk_add_f32 v[178:179], v[178:179], v[138:139]
	v_pk_add_f32 v[180:181], v[180:181], v[140:141]
	v_pk_add_f32 v[182:183], v[182:183], v[142:143]
	v_pk_add_f32 v[176:177], v[176:177], v[120:121] neg_lo:[0,1] neg_hi:[0,1]
	v_pk_add_f32 v[178:179], v[178:179], v[122:123] neg_lo:[0,1] neg_hi:[0,1]
	v_pk_add_f32 v[180:181], v[180:181], v[124:125] neg_lo:[0,1] neg_hi:[0,1]
	v_pk_add_f32 v[182:183], v[182:183], v[126:127] neg_lo:[0,1] neg_hi:[0,1]
	v_pk_fma_f32 v[194:195], v[176:177], v[192:193], v[136:137] neg_lo:[0,0,1] neg_hi:[0,0,1]
	v_pk_fma_f32 v[196:197], v[178:179], v[192:193], v[138:139] neg_lo:[0,0,1] neg_hi:[0,0,1]
	v_pk_fma_f32 v[198:199], v[180:181], v[192:193], v[140:141] neg_lo:[0,0,1] neg_hi:[0,0,1]
	v_pk_fma_f32 v[200:201], v[182:183], v[192:193], v[142:143] neg_lo:[0,0,1] neg_hi:[0,0,1]
	v_cvt_pk_bf16_f32 v188, v194, v195
	v_cvt_pk_bf16_f32 v189, v196, v197
	v_cvt_pk_bf16_f32 v190, v198, v199
	v_cvt_pk_bf16_f32 v191, v200, v201
	global_store_dwordx4 v7, v[188:191], s[14:15]
	s_add_u32 s14, s14, 0x800
	s_addc_u32 s15, s15, 0
	s_waitcnt vmcnt(7)
	v_lshlrev_b32_e32 v144, 16, v30
	v_and_b32_e32 v145, 0xffff0000, v30
	v_lshlrev_b32_e32 v146, 16, v31
	v_and_b32_e32 v147, 0xffff0000, v31
	v_lshlrev_b32_e32 v148, 16, v32
	v_and_b32_e32 v149, 0xffff0000, v32
	v_lshlrev_b32_e32 v150, 16, v33
	v_and_b32_e32 v151, 0xffff0000, v33
	v_pk_add_f32 v[176:177], v[176:177], v[144:145]
	v_pk_add_f32 v[178:179], v[178:179], v[146:147]
	v_pk_add_f32 v[180:181], v[180:181], v[148:149]
	v_pk_add_f32 v[182:183], v[182:183], v[150:151]
	v_pk_add_f32 v[176:177], v[176:177], v[128:129] neg_lo:[0,1] neg_hi:[0,1]
	v_pk_add_f32 v[178:179], v[178:179], v[130:131] neg_lo:[0,1] neg_hi:[0,1]
	v_pk_add_f32 v[180:181], v[180:181], v[132:133] neg_lo:[0,1] neg_hi:[0,1]
	v_pk_add_f32 v[182:183], v[182:183], v[134:135] neg_lo:[0,1] neg_hi:[0,1]
	v_pk_fma_f32 v[194:195], v[176:177], v[192:193], v[144:145] neg_lo:[0,0,1] neg_hi:[0,0,1]
	v_pk_fma_f32 v[196:197], v[178:179], v[192:193], v[146:147] neg_lo:[0,0,1] neg_hi:[0,0,1]
	v_pk_fma_f32 v[198:199], v[180:181], v[192:193], v[148:149] neg_lo:[0,0,1] neg_hi:[0,0,1]
	v_pk_fma_f32 v[200:201], v[182:183], v[192:193], v[150:151] neg_lo:[0,0,1] neg_hi:[0,0,1]
	v_cvt_pk_bf16_f32 v184, v194, v195
	v_cvt_pk_bf16_f32 v185, v196, v197
	v_cvt_pk_bf16_f32 v186, v198, v199
	v_cvt_pk_bf16_f32 v187, v200, v201
	global_store_dwordx4 v7, v[184:187], s[14:15]
	s_add_u32 s14, s14, 0x800
	s_addc_u32 s15, s15, 0
	s_waitcnt vmcnt(7)
	v_lshlrev_b32_e32 v152, 16, v34
	v_and_b32_e32 v153, 0xffff0000, v34
	v_lshlrev_b32_e32 v154, 16, v35
	v_and_b32_e32 v155, 0xffff0000, v35
	v_lshlrev_b32_e32 v156, 16, v36
	v_and_b32_e32 v157, 0xffff0000, v36
	v_lshlrev_b32_e32 v158, 16, v37
	v_and_b32_e32 v159, 0xffff0000, v37
	v_pk_add_f32 v[176:177], v[176:177], v[152:153]
	v_pk_add_f32 v[178:179], v[178:179], v[154:155]
	v_pk_add_f32 v[180:181], v[180:181], v[156:157]
	v_pk_add_f32 v[182:183], v[182:183], v[158:159]
	v_pk_add_f32 v[176:177], v[176:177], v[136:137] neg_lo:[0,1] neg_hi:[0,1]
	v_pk_add_f32 v[178:179], v[178:179], v[138:139] neg_lo:[0,1] neg_hi:[0,1]
	v_pk_add_f32 v[180:181], v[180:181], v[140:141] neg_lo:[0,1] neg_hi:[0,1]
	v_pk_add_f32 v[182:183], v[182:183], v[142:143] neg_lo:[0,1] neg_hi:[0,1]
	v_pk_fma_f32 v[194:195], v[176:177], v[192:193], v[152:153] neg_lo:[0,0,1] neg_hi:[0,0,1]
	v_pk_fma_f32 v[196:197], v[178:179], v[192:193], v[154:155] neg_lo:[0,0,1] neg_hi:[0,0,1]
	v_pk_fma_f32 v[198:199], v[180:181], v[192:193], v[156:157] neg_lo:[0,0,1] neg_hi:[0,0,1]
	v_pk_fma_f32 v[200:201], v[182:183], v[192:193], v[158:159] neg_lo:[0,0,1] neg_hi:[0,0,1]
	v_cvt_pk_bf16_f32 v188, v194, v195
	v_cvt_pk_bf16_f32 v189, v196, v197
	v_cvt_pk_bf16_f32 v190, v198, v199
	v_cvt_pk_bf16_f32 v191, v200, v201
	global_store_dwordx4 v7, v[188:191], s[14:15]
	s_add_u32 s14, s14, 0x800
	s_addc_u32 s15, s15, 0
	s_waitcnt vmcnt(7)
	v_lshlrev_b32_e32 v160, 16, v38
	v_and_b32_e32 v161, 0xffff0000, v38
	v_lshlrev_b32_e32 v162, 16, v39
	v_and_b32_e32 v163, 0xffff0000, v39
	v_lshlrev_b32_e32 v164, 16, v40
	v_and_b32_e32 v165, 0xffff0000, v40
	v_lshlrev_b32_e32 v166, 16, v41
	v_and_b32_e32 v167, 0xffff0000, v41
	v_pk_add_f32 v[176:177], v[176:177], v[160:161]
	v_pk_add_f32 v[178:179], v[178:179], v[162:163]
	v_pk_add_f32 v[180:181], v[180:181], v[164:165]
	v_pk_add_f32 v[182:183], v[182:183], v[166:167]
	v_pk_add_f32 v[176:177], v[176:177], v[144:145] neg_lo:[0,1] neg_hi:[0,1]
	v_pk_add_f32 v[178:179], v[178:179], v[146:147] neg_lo:[0,1] neg_hi:[0,1]
	v_pk_add_f32 v[180:181], v[180:181], v[148:149] neg_lo:[0,1] neg_hi:[0,1]
	v_pk_add_f32 v[182:183], v[182:183], v[150:151] neg_lo:[0,1] neg_hi:[0,1]
	v_pk_fma_f32 v[194:195], v[176:177], v[192:193], v[160:161] neg_lo:[0,0,1] neg_hi:[0,0,1]
	v_pk_fma_f32 v[196:197], v[178:179], v[192:193], v[162:163] neg_lo:[0,0,1] neg_hi:[0,0,1]
	v_pk_fma_f32 v[198:199], v[180:181], v[192:193], v[164:165] neg_lo:[0,0,1] neg_hi:[0,0,1]
	v_pk_fma_f32 v[200:201], v[182:183], v[192:193], v[166:167] neg_lo:[0,0,1] neg_hi:[0,0,1]
	v_cvt_pk_bf16_f32 v184, v194, v195
	v_cvt_pk_bf16_f32 v185, v196, v197
	v_cvt_pk_bf16_f32 v186, v198, v199
	v_cvt_pk_bf16_f32 v187, v200, v201
	global_store_dwordx4 v7, v[184:187], s[14:15]
	s_add_u32 s14, s14, 0x800
	s_addc_u32 s15, s15, 0
	s_waitcnt vmcnt(7)
	v_lshlrev_b32_e32 v168, 16, v42
	v_and_b32_e32 v169, 0xffff0000, v42
	v_lshlrev_b32_e32 v170, 16, v43
	v_and_b32_e32 v171, 0xffff0000, v43
	v_lshlrev_b32_e32 v172, 16, v44
	v_and_b32_e32 v173, 0xffff0000, v44
	v_lshlrev_b32_e32 v174, 16, v45
	v_and_b32_e32 v175, 0xffff0000, v45
	v_pk_add_f32 v[176:177], v[176:177], v[168:169]
	v_pk_add_f32 v[178:179], v[178:179], v[170:171]
	v_pk_add_f32 v[180:181], v[180:181], v[172:173]
	v_pk_add_f32 v[182:183], v[182:183], v[174:175]
	v_pk_add_f32 v[176:177], v[176:177], v[152:153] neg_lo:[0,1] neg_hi:[0,1]
	v_pk_add_f32 v[178:179], v[178:179], v[154:155] neg_lo:[0,1] neg_hi:[0,1]
	v_pk_add_f32 v[180:181], v[180:181], v[156:157] neg_lo:[0,1] neg_hi:[0,1]
	v_pk_add_f32 v[182:183], v[182:183], v[158:159] neg_lo:[0,1] neg_hi:[0,1]
	v_pk_fma_f32 v[194:195], v[176:177], v[192:193], v[168:169] neg_lo:[0,0,1] neg_hi:[0,0,1]
	v_pk_fma_f32 v[196:197], v[178:179], v[192:193], v[170:171] neg_lo:[0,0,1] neg_hi:[0,0,1]
	v_pk_fma_f32 v[198:199], v[180:181], v[192:193], v[172:173] neg_lo:[0,0,1] neg_hi:[0,0,1]
	v_pk_fma_f32 v[200:201], v[182:183], v[192:193], v[174:175] neg_lo:[0,0,1] neg_hi:[0,0,1]
	v_cvt_pk_bf16_f32 v188, v194, v195
	v_cvt_pk_bf16_f32 v189, v196, v197
	v_cvt_pk_bf16_f32 v190, v198, v199
	v_cvt_pk_bf16_f32 v191, v200, v201
	global_store_dwordx4 v7, v[188:191], s[14:15]
; __device__ __forceinline__ void xcd_barrier(const XcdBarrier& b) {
;     asm volatile("s_waitcnt vmcnt(0)" ::: "memory");
;     __syncthreads();
;     if (threadIdx.x == 0) {
;         unsigned* bar = b.bar;
;         __builtin_amdgcn_s_waitcnt(0);
;         unsigned nloc = b.st[0], nx = b.st[1];
;         if (nloc == 0u) { xcd_barrier_complete(bar, b.x, nloc, nx); b.st[0] = nloc; b.st[1] = nx; }
.Lpd2_next:
	s_add_u32 s8, s8, s20
	s_branch .Lpd2_loop
.Lpd2_done:
	s_and_b64 vcc, exec, s[38:39]
	s_cbranch_vccz .LBB0_479
	s_mov_b64 s[44:45], s[40:41]
	s_mov_b32 s33, s93
	s_waitcnt vmcnt(0)
	v_cmp_eq_u32_e32 vcc, 0, v0
	s_barrier
	s_and_saveexec_b64 s[42:43], vcc
	s_cbranch_execz .LBB0_478
	v_mov_b32_e32 v1, s84
	s_waitcnt vmcnt(0) expcnt(0) lgkmcnt(0)
	ds_read_b32 v4, v1
	ds_read_b32 v2, v1 offset:4
	s_waitcnt lgkmcnt(1)
	v_cmp_ne_u32_e32 vcc, 0, v4
	s_cbranch_vccnz .LBB0_449
	s_load_dwordx2 s[4:5], s[2:3], 0x4
	s_add_u32 s6, s44, 0x1000
	s_addc_u32 s7, s45, 0
	s_add_u32 s8, s44, 0x1100
	s_addc_u32 s9, s45, 0
	s_waitcnt lgkmcnt(0)
	s_mul_i32 s22, s4, s16
	s_add_u32 s4, s44, 0x1200
	s_mul_i32 s22, s22, s5
	s_addc_u32 s5, s45, 0
	s_add_u32 s10, s44, 0x1300
	s_addc_u32 s11, s45, 0
	s_mov_b32 s23, 1
	s_mov_b64 s[2:3], 0
	v_mov_b64_e32 v[2:3], s[44:45]
	v_mov_b64_e32 v[4:5], s[6:7]
	v_mov_b64_e32 v[6:7], s[8:9]
	v_mov_b64_e32 v[8:9], s[4:5]
	v_mov_b64_e32 v[10:11], s[10:11]
	s_branch .LBB0_439
